# SwiGLU epilogues: four 16-byte H8 stores per lane (v_permlane16_swap between lane pairs) instead of eight 8-byte stores; in-epilogue vmcnt waits recounted for the new store count
# baseline (speedup 1.0000x reference)
; __device__ __forceinline__ float rstd_fin4(const f32x4 a) { float s = (a[0] + a[1]) + (a[2] + a[3]); s += __shfl_xor(s, 16); s += __shfl_xor(s, 32); return __builtin_amdgcn_rsqf(s * (1.f / 1024.f) + 1e-6f); }
;     __device__ __forceinline__ void operator()(const f32x4 (&acc)[2][2][4][2], const Unit& u, int wr, int wc, int fr, int fq) const {
;         asm volatile("" : "+v"(fr), "+v"(fq));
;         const int row0 = u.pm * BM + wr * 64 + fr;
;         unsigned char* const hb = (unsigned char*)H + (size_t)(u.pm * (FFH / 128) + u.pn + pn0) * 32768 + (((wr * 4 + wc) * 8) * 64 + (fq >> 1) * 32 + fr * 2 + (fq & 1)) * 8;
;         f32x4 pa[2][4];
; #pragma unroll
;         for (int ai = 0; ai < 2; ++ai)
; #pragma unroll
;             for (int m = 0; m < 4; ++m) pa[ai][m] = rstd_ld4(ss, row0 + ai * HALF + m * 16, fq);
; #pragma unroll
;         for (int ai = 0; ai < 2; ++ai)
; #pragma unroll
;             for (int m = 0; m < 4; ++m) { const float rs = rstd_fin4(pa[ai][m]) * sc;
;                 const float rsl = rs * 1.4426950408889634f, rsu = rs * 0.6931471805599453f;
;                 f32x4 h0, h1;
; #pragma unroll
;                 for (int n = 0; n < 2; ++n) { const f32x4 G = acc[ai][0][m][n], U = acc[ai][1][m][n]; f32x4 hv;
; #pragma unroll
;                     for (int q = 0; q < 2; ++q) { const f32x2 g2 = (f32x2){G[2 * q], G[2 * q + 1]} * rsl, u2 = (f32x2){U[2 * q], U[2 * q + 1]} * rsu;
;                         f32x2 r2; r2.x = __builtin_amdgcn_rcpf(1.f + __builtin_amdgcn_exp2f(-g2.x)); r2.y = __builtin_amdgcn_rcpf(1.f + __builtin_amdgcn_exp2f(-g2.y));
;                         const f32x2 o2 = g2 * u2 * r2; hv[2 * q] = o2.x; hv[2 * q + 1] = o2.y; }
;                     if (n == 0) h0 = hv; else h1 = hv; }
;                 unsigned w0 = 0u, w1 = 0u;
;                 w0 = __builtin_amdgcn_cvt_pk_fp8_f32(h0[0], h0[1], w0, false); w0 = __builtin_amdgcn_cvt_pk_fp8_f32(h0[2], h0[3], w0, true); w1 = __builtin_amdgcn_cvt_pk_fp8_f32(h1[0], h1[1], w1, false); w1 = __builtin_amdgcn_cvt_pk_fp8_f32(h1[2], h1[3], w1, true);
;                 *(u32x2*)(hb + (ai * 4 + m) * 512) = (u32x2){w0, w1}; asm volatile("" ::: "memory"); }
.LBB0_434:
	s_lshl_b32 s4, s71, 8
	v_mov_b32_e32 v142, v1
	v_mov_b32_e32 v143, v164
	s_add_i32 s4, s4, s47
	v_and_b32_e32 v145, 64, v246
	v_add_u32_e32 v132, s4, v142
	v_lshlrev_b32_e32 v134, 2, v143
	v_ashrrev_i32_e32 v135, 31, v134
	v_ashrrev_i32_e32 v133, 31, v132
	v_lshl_add_u64 v[134:135], v[134:135], 2, s[48:49]
	v_lshlrev_b64 v[132:133], 6, v[132:133]
	v_lshl_add_u64 v[140:141], v[134:135], 0, v[132:133]
	global_load_dwordx4 v[132:135], v[140:141], off
	global_load_dwordx4 v[136:139], v[140:141], off offset:1024
	global_load_dwordx4 v[170:173], v[140:141], off offset:2048
	global_load_dwordx4 v[148:151], v[140:141], off offset:3072
	v_xor_b32_e32 v144, 16, v246
	v_add_u32_e32 v145, 64, v145
	v_xor_b32_e32 v146, 32, v246
	v_cmp_lt_i32_e32 vcc, v144, v145
	s_mul_i32 s4, s71, 22
	s_add_i32 s4, s4, s70
	v_cndmask_b32_e32 v144, v246, v144, vcc
	v_cmp_lt_i32_e32 vcc, v146, v145
	v_lshlrev_b32_e32 v168, 2, v144
	s_ashr_i32 s5, s4, 31
	v_cndmask_b32_e32 v145, v246, v146, vcc
	v_lshlrev_b32_e32 v167, 2, v145
	v_lshlrev_b32_e32 v147, 4, v143
	v_lshl_add_u32 v142, v142, 1, s68
	s_lshl_b64 s[4:5], s[4:5], 15
	v_and_b32_e32 v146, 0x1fffffe0, v147
	v_and_or_b32 v142, v143, 1, v142
	v_add_lshl_u32 v142, v142, v146, 3
	s_add_u32 s4, s22, s4
	v_ashrrev_i32_e32 v143, 31, v142
	s_addc_u32 s5, s23, s5
	v_lshl_add_u64 v[162:163], s[4:5], 0, v[142:143]
	v_mov_b32_e32 v174, v3
	v_mov_b32_e32 v175, v3
	s_mov_b64 s[4:5], -1
	s_waitcnt vmcnt(0)
	v_mov_b32_e32 v144, v133
	v_mov_b32_e32 v145, v134
	v_mov_b32_e32 v133, v135
	v_mov_b32_e32 v134, v137
	v_mov_b32_e32 v135, v138
	v_mov_b32_e32 v137, v139
	v_pk_add_f32 v[134:135], v[134:135], v[136:137]
	v_pk_add_f32 v[132:133], v[144:145], v[132:133]
	v_add_f32_e32 v134, v134, v135
	v_add_f32_e32 v136, v132, v133
	ds_bpermute_b32 v137, v168, v134
	ds_bpermute_b32 v135, v168, v136
	v_add_co_u32_e32 v132, vcc, s88, v140
	s_waitcnt lgkmcnt(1)
	v_add_f32_e32 v134, v134, v137
	s_waitcnt lgkmcnt(0)
	v_add_f32_e32 v135, v136, v135
	ds_bpermute_b32 v137, v167, v134
	ds_bpermute_b32 v136, v167, v135
	v_addc_co_u32_e32 v133, vcc, 0, v141, vcc
	global_load_dwordx4 v[144:147], v[132:133], off
	global_load_dwordx4 v[140:143], v[132:133], off offset:1024
	s_waitcnt lgkmcnt(1)
	v_add_f32_e32 v134, v134, v137
	s_waitcnt lgkmcnt(0)
	v_add_f32_e32 v135, v135, v136
	v_fmamk_f32 v134, v134, 0x3a800000, v227
	v_fmamk_f32 v135, v135, 0x3a800000, v227
	v_rsq_f32_e32 v177, v134
	v_rsq_f32_e32 v169, v135
	global_load_dwordx4 v[136:139], v[132:133], off offset:2048
	s_nop 0
	global_load_dwordx4 v[132:135], v[132:133], off offset:3072
	s_andn2_b64 vcc, exec, s[38:39]
	v_mul_f32_e32 v180, 0x3fb8aa3b, v177
	v_mul_f32_e32 v182, 0x3f317218, v177
	v_mul_f32_e32 v176, 0x3fb8aa3b, v169
	v_mul_f32_e32 v178, 0x3f317218, v169
	v_pk_mul_f32 v[112:113], v[112:113], v[180:181] op_sel_hi:[1,0]
	v_pk_mul_f32 v[104:105], v[104:105], v[182:183] op_sel_hi:[1,0]
	v_pk_mul_f32 v[128:129], v[128:129], v[176:177] op_sel_hi:[1,0]
	v_pk_mul_f32 v[120:121], v[120:121], v[178:179] op_sel_hi:[1,0]
	v_pk_mul_f32 v[130:131], v[130:131], v[176:177] op_sel_hi:[1,0]
	v_pk_mul_f32 v[122:123], v[122:123], v[178:179] op_sel_hi:[1,0]
	v_pk_mul_f32 v[124:125], v[124:125], v[176:177] op_sel_hi:[1,0]
	v_pk_mul_f32 v[116:117], v[116:117], v[178:179] op_sel_hi:[1,0]
	v_pk_mul_f32 v[126:127], v[126:127], v[176:177] op_sel_hi:[1,0]
	v_pk_mul_f32 v[118:119], v[118:119], v[178:179] op_sel_hi:[1,0]
	v_exp_f32_e64 v177, -v112
	v_exp_f32_e64 v178, -v113
	v_pk_mul_f32 v[104:105], v[112:113], v[104:105]
	v_pk_mul_f32 v[112:113], v[114:115], v[180:181] op_sel_hi:[1,0]
	v_pk_mul_f32 v[106:107], v[106:107], v[182:183] op_sel_hi:[1,0]
	v_exp_f32_e64 v114, -v112
	v_exp_f32_e64 v115, -v113
	v_pk_mul_f32 v[108:109], v[108:109], v[180:181] op_sel_hi:[1,0]
	v_pk_mul_f32 v[106:107], v[112:113], v[106:107]
	v_add_f32_e32 v114, 1.0, v114
	v_add_f32_e32 v115, 1.0, v115
	v_exp_f32_e64 v112, -v108
	v_exp_f32_e64 v113, -v109
	v_rcp_f32_e32 v114, v114
	v_rcp_f32_e32 v115, v115
	v_exp_f32_e64 v169, -v128
	v_exp_f32_e64 v176, -v129
	v_pk_mul_f32 v[120:121], v[128:129], v[120:121]
	v_exp_f32_e64 v128, -v130
	v_exp_f32_e64 v129, -v131
	v_pk_mul_f32 v[122:123], v[130:131], v[122:123]
	v_exp_f32_e64 v130, -v124
	v_exp_f32_e64 v131, -v125
	v_pk_mul_f32 v[116:117], v[124:125], v[116:117]
	v_exp_f32_e64 v124, -v126
	v_exp_f32_e64 v125, -v127
	v_add_f32_e32 v112, 1.0, v112
	v_add_f32_e32 v113, 1.0, v113
	v_pk_mul_f32 v[110:111], v[110:111], v[180:181] op_sel_hi:[1,0]
	v_pk_mul_f32 v[106:107], v[106:107], v[114:115]
	v_rcp_f32_e32 v112, v112
	v_rcp_f32_e32 v113, v113
	v_exp_f32_e64 v114, -v110
	v_pk_mul_f32 v[100:101], v[100:101], v[182:183] op_sel_hi:[1,0]
	v_pk_mul_f32 v[118:119], v[126:127], v[118:119]
	v_add_f32_e32 v126, 1.0, v169
	v_add_f32_e32 v127, 1.0, v176
	v_pk_mul_f32 v[100:101], v[108:109], v[100:101]
	v_mov_b32_e32 v108, v171
	v_mov_b32_e32 v109, v172
	v_mov_b32_e32 v171, v173
	v_add_f32_e32 v169, 1.0, v124
	v_add_f32_e32 v176, 1.0, v125
	v_rcp_f32_e32 v124, v126
	v_rcp_f32_e32 v125, v127
	v_pk_add_f32 v[108:109], v[108:109], v[170:171]
	v_pk_mul_f32 v[100:101], v[100:101], v[112:113]
	v_add_f32_e32 v112, 1.0, v114
	v_add_f32_e32 v114, v108, v109
	v_add_f32_e32 v128, 1.0, v128
	v_add_f32_e32 v129, 1.0, v129
	v_add_f32_e32 v130, 1.0, v130
	v_add_f32_e32 v131, 1.0, v131
	ds_bpermute_b32 v115, v168, v114
	v_rcp_f32_e32 v126, v128
	v_rcp_f32_e32 v127, v129
	v_rcp_f32_e32 v128, v130
	v_rcp_f32_e32 v129, v131
	v_pk_mul_f32 v[120:121], v[120:121], v[124:125]
	v_exp_f32_e64 v113, -v111
	v_cvt_pk_fp8_f32 v174, v120, v121
	v_pk_mul_f32 v[116:117], v[116:117], v[128:129]
	v_rcp_f32_e32 v108, v112
	s_waitcnt lgkmcnt(0)
; __device__ __forceinline__ float rstd_fin4(const f32x4 a) { float s = (a[0] + a[1]) + (a[2] + a[3]); s += __shfl_xor(s, 16); s += __shfl_xor(s, 32); return __builtin_amdgcn_rsqf(s * (1.f / 1024.f) + 1e-6f); }
;     __device__ __forceinline__ void operator()(const f32x4 (&acc)[2][2][4][2], const Unit& u, int wr, int wc, int fr, int fq) const {
;     ...
;             for (int m = 0; m < 4; ++m) { const float rs = rstd_fin4(pa[ai][m]) * sc;
;                 const float rsl = rs * 1.4426950408889634f, rsu = rs * 0.6931471805599453f;
;                 f32x4 h0, h1;
; #pragma unroll
;                 for (int n = 0; n < 2; ++n) { const f32x4 G = acc[ai][0][m][n], U = acc[ai][1][m][n]; f32x4 hv;
; #pragma unroll
;                     for (int q = 0; q < 2; ++q) { const f32x2 g2 = (f32x2){G[2 * q], G[2 * q + 1]} * rsl, u2 = (f32x2){U[2 * q], U[2 * q + 1]} * rsu;
;                         f32x2 r2; r2.x = __builtin_amdgcn_rcpf(1.f + __builtin_amdgcn_exp2f(-g2.x)); r2.y = __builtin_amdgcn_rcpf(1.f + __builtin_amdgcn_exp2f(-g2.y));
;                         const f32x2 o2 = g2 * u2 * r2; hv[2 * q] = o2.x; hv[2 * q + 1] = o2.y; }
;                     if (n == 0) h0 = hv; else h1 = hv; }
;                 unsigned w0 = 0u, w1 = 0u;
;                 w0 = __builtin_amdgcn_cvt_pk_fp8_f32(h0[0], h0[1], w0, false); w0 = __builtin_amdgcn_cvt_pk_fp8_f32(h0[2], h0[3], w0, true); w1 = __builtin_amdgcn_cvt_pk_fp8_f32(h1[0], h1[1], w1, false); w1 = __builtin_amdgcn_cvt_pk_fp8_f32(h1[2], h1[3], w1, true);
;                 *(u32x2*)(hb + (ai * 4 + m) * 512) = (u32x2){w0, w1}; asm volatile("" ::: "memory"); }
	v_add_f32_e32 v112, v114, v115
	v_cvt_pk_fp8_f32 v175, v116, v117
	v_pk_mul_f32 v[116:117], v[122:123], v[126:127]
	v_add_f32_e32 v109, 1.0, v113
	ds_bpermute_b32 v113, v167, v112
	v_cvt_pk_fp8_f32 v174, v116, v117 op_sel:[0,0,1]
	v_add_f32_e32 v116, 1.0, v177
	v_add_f32_e32 v117, 1.0, v178
	v_rcp_f32_e32 v116, v116
	v_rcp_f32_e32 v117, v117
	v_pk_mul_f32 v[102:103], v[102:103], v[182:183] op_sel_hi:[1,0]
	v_rcp_f32_e32 v109, v109
	v_pk_mul_f32 v[102:103], v[110:111], v[102:103]
	v_mov_b32_e32 v111, v3
	v_cvt_pk_fp8_f32 v111, v100, v101
	s_waitcnt lgkmcnt(0)
	v_add_f32_e32 v100, v112, v113
	v_pk_mul_f32 v[104:105], v[104:105], v[116:117]
	v_mov_b32_e32 v110, v3
	v_fmamk_f32 v100, v100, 0x3a800000, v227
	v_cvt_pk_fp8_f32 v110, v104, v105
	v_rsq_f32_e32 v104, v100
	v_pk_mul_f32 v[100:101], v[102:103], v[108:109]
	v_rcp_f32_e32 v130, v169
	v_cvt_pk_fp8_f32 v111, v100, v101 op_sel:[0,0,1]
	v_mul_f32_e32 v100, 0x3fb8aa3b, v104
	v_pk_mul_f32 v[96:97], v[96:97], v[100:101] op_sel_hi:[1,0]
	v_mul_f32_e32 v102, 0x3f317218, v104
	v_exp_f32_e64 v101, -v96
	v_exp_f32_e64 v103, -v97
	v_rcp_f32_e32 v131, v176
	v_cvt_pk_fp8_f32 v110, v106, v107 op_sel:[0,0,1]
	v_add_f32_e32 v101, 1.0, v101
	v_pk_mul_f32 v[88:89], v[88:89], v[102:103] op_sel_hi:[1,0]
	v_rcp_f32_e32 v104, v101
	v_add_f32_e32 v101, 1.0, v103
	v_pk_mul_f32 v[88:89], v[96:97], v[88:89]
	v_pk_mul_f32 v[96:97], v[98:99], v[100:101] op_sel_hi:[1,0]
	v_pk_mul_f32 v[90:91], v[90:91], v[102:103] op_sel_hi:[1,0]
	v_pk_mul_f32 v[92:93], v[92:93], v[100:101] op_sel_hi:[1,0]
	v_exp_f32_e64 v98, -v96
	v_exp_f32_e64 v99, -v97
	v_pk_mul_f32 v[90:91], v[96:97], v[90:91]
	v_exp_f32_e64 v96, -v92
	v_exp_f32_e64 v97, -v93
	v_add_f32_e32 v98, 1.0, v98
	v_add_f32_e32 v99, 1.0, v99
	v_add_f32_e32 v96, 1.0, v96
	v_add_f32_e32 v97, 1.0, v97
	v_rcp_f32_e32 v96, v96
	v_rcp_f32_e32 v97, v97
	v_rcp_f32_e32 v98, v98
	v_rcp_f32_e32 v99, v99
	v_pk_mul_f32 v[84:85], v[84:85], v[102:103] op_sel_hi:[1,0]
	v_rcp_f32_e32 v105, v101
	v_pk_mul_f32 v[84:85], v[92:93], v[84:85]
	v_pk_mul_f32 v[90:91], v[90:91], v[98:99]
	v_pk_mul_f32 v[84:85], v[84:85], v[96:97]
	v_mov_b32_e32 v96, v149
	v_mov_b32_e32 v97, v150
	v_mov_b32_e32 v149, v151
	v_pk_add_f32 v[96:97], v[96:97], v[148:149]
	v_pk_mul_f32 v[92:93], v[94:95], v[100:101] op_sel_hi:[1,0]
	v_add_f32_e32 v98, v96, v97
	ds_bpermute_b32 v99, v168, v98
	v_exp_f32_e64 v94, -v92
	v_exp_f32_e64 v95, -v93
	v_pk_mul_f32 v[88:89], v[88:89], v[104:105]
	v_mov_b32_e32 v96, v3
	v_add_f32_e32 v94, 1.0, v94
	v_add_f32_e32 v95, 1.0, v95
	v_cvt_pk_fp8_f32 v96, v88, v89
	s_waitcnt lgkmcnt(0)
	v_add_f32_e32 v88, v98, v99
	v_rcp_f32_e32 v94, v94
	v_rcp_f32_e32 v95, v95
	v_mov_b32_e32 v97, v3
	ds_bpermute_b32 v89, v167, v88
	v_cvt_pk_fp8_f32 v97, v84, v85
	v_pk_mul_f32 v[86:87], v[86:87], v[102:103] op_sel_hi:[1,0]
	v_pk_mul_f32 v[118:119], v[118:119], v[130:131]
	v_pk_mul_f32 v[84:85], v[92:93], v[86:87]
	v_cvt_pk_fp8_f32 v175, v118, v119 op_sel:[0,0,1]
	v_pk_mul_f32 v[84:85], v[84:85], v[94:95]
	v_cvt_pk_fp8_f32 v96, v90, v91 op_sel:[0,0,1]
	v_cvt_pk_fp8_f32 v97, v84, v85 op_sel:[0,0,1]
	s_waitcnt lgkmcnt(0)
	v_add_f32_e32 v84, v88, v89
	v_fmamk_f32 v84, v84, 0x3a800000, v227
	v_rsq_f32_e32 v85, v84
	v_and_b32_e32 v218, 16, v246
	v_mov_b32_e32 v219, 0x200
	v_cmp_eq_u32_e64 s[60:61], 0, v218
	s_nop 1
	v_cndmask_b32_e64 v218, -8, v219, s[60:61]
	v_ashrrev_i32_e32 v219, 31, v218
	v_lshl_add_u64 v[216:217], v[162:163], 0, v[218:219]
	v_mov_b32_e32 v210, v174
	v_mov_b32_e32 v211, v175
	v_mov_b32_e32 v208, v110
	v_mov_b32_e32 v209, v111
	s_nop 1
	v_permlane16_swap_b32_e32 v208, v210
	v_permlane16_swap_b32_e32 v209, v211
	global_store_dwordx4 v[216:217], v[208:211], off
	v_mul_f32_e32 v84, 0x3fb8aa3b, v85
	v_pk_mul_f32 v[80:81], v[80:81], v[84:85] op_sel_hi:[1,0]
	v_mul_f32_e32 v86, 0x3f317218, v85
	v_exp_f32_e64 v87, -v80
	v_exp_f32_e64 v85, -v81
	v_mov_b32_e32 v214, v96
	v_mov_b32_e32 v215, v97
	v_pk_mul_f32 v[72:73], v[72:73], v[86:87] op_sel_hi:[1,0]
	v_add_f32_e32 v87, 1.0, v87
	v_add_f32_e32 v85, 1.0, v85
	v_pk_mul_f32 v[72:73], v[80:81], v[72:73]
	v_pk_mul_f32 v[80:81], v[82:83], v[84:85] op_sel_hi:[1,0]
	v_pk_mul_f32 v[74:75], v[74:75], v[86:87] op_sel_hi:[1,0]
	v_pk_mul_f32 v[76:77], v[76:77], v[84:85] op_sel_hi:[1,0]
	v_exp_f32_e64 v82, -v80
	v_exp_f32_e64 v83, -v81
	v_pk_mul_f32 v[74:75], v[80:81], v[74:75]
	v_exp_f32_e64 v80, -v76
	v_exp_f32_e64 v81, -v77
	v_add_f32_e32 v82, 1.0, v82
	v_add_f32_e32 v83, 1.0, v83
	v_add_f32_e32 v80, 1.0, v80
	v_add_f32_e32 v81, 1.0, v81
	v_rcp_f32_e32 v80, v80
	v_rcp_f32_e32 v81, v81
	v_rcp_f32_e32 v82, v82
	v_rcp_f32_e32 v83, v83
	v_pk_mul_f32 v[68:69], v[68:69], v[86:87] op_sel_hi:[1,0]
	v_rcp_f32_e32 v88, v87
	v_pk_mul_f32 v[68:69], v[76:77], v[68:69]
	v_pk_mul_f32 v[74:75], v[74:75], v[82:83]
	v_pk_mul_f32 v[68:69], v[68:69], v[80:81]
	s_waitcnt vmcnt(4)
	v_mov_b32_e32 v80, v145
	v_mov_b32_e32 v81, v146
	v_mov_b32_e32 v145, v147
	v_pk_add_f32 v[80:81], v[80:81], v[144:145]
	v_rcp_f32_e32 v89, v85
	v_add_f32_e32 v82, v80, v81
	v_pk_mul_f32 v[76:77], v[78:79], v[84:85] op_sel_hi:[1,0]
	ds_bpermute_b32 v83, v168, v82
	v_exp_f32_e64 v78, -v76
	v_exp_f32_e64 v79, -v77
	v_pk_mul_f32 v[72:73], v[72:73], v[88:89]
	v_mov_b32_e32 v80, v3
	v_add_f32_e32 v78, 1.0, v78
	v_add_f32_e32 v79, 1.0, v79
	v_cvt_pk_fp8_f32 v80, v72, v73
	s_waitcnt lgkmcnt(0)
	v_add_f32_e32 v72, v82, v83
	v_rcp_f32_e32 v78, v78
	v_rcp_f32_e32 v79, v79
	v_mov_b32_e32 v81, v3
	ds_bpermute_b32 v73, v167, v72
	v_cvt_pk_fp8_f32 v81, v68, v69
	v_pk_mul_f32 v[70:71], v[70:71], v[86:87] op_sel_hi:[1,0]
	v_cvt_pk_fp8_f32 v80, v74, v75 op_sel:[0,0,1]
	v_pk_mul_f32 v[68:69], v[76:77], v[70:71]
	s_nop 0
	v_pk_mul_f32 v[68:69], v[68:69], v[78:79]
	s_nop 0
	v_cvt_pk_fp8_f32 v81, v68, v69 op_sel:[0,0,1]
	s_waitcnt lgkmcnt(0)
; __device__ __forceinline__ float rstd_fin4(const f32x4 a) { float s = (a[0] + a[1]) + (a[2] + a[3]); s += __shfl_xor(s, 16); s += __shfl_xor(s, 32); return __builtin_amdgcn_rsqf(s * (1.f / 1024.f) + 1e-6f); }
;     __device__ __forceinline__ void operator()(const f32x4 (&acc)[2][2][4][2], const Unit& u, int wr, int wc, int fr, int fq) const {
;     ...
;             for (int m = 0; m < 4; ++m) { const float rs = rstd_fin4(pa[ai][m]) * sc;
;                 const float rsl = rs * 1.4426950408889634f, rsu = rs * 0.6931471805599453f;
;                 f32x4 h0, h1;
; #pragma unroll
;                 for (int n = 0; n < 2; ++n) { const f32x4 G = acc[ai][0][m][n], U = acc[ai][1][m][n]; f32x4 hv;
; #pragma unroll
;                     for (int q = 0; q < 2; ++q) { const f32x2 g2 = (f32x2){G[2 * q], G[2 * q + 1]} * rsl, u2 = (f32x2){U[2 * q], U[2 * q + 1]} * rsu;
;                         f32x2 r2; r2.x = __builtin_amdgcn_rcpf(1.f + __builtin_amdgcn_exp2f(-g2.x)); r2.y = __builtin_amdgcn_rcpf(1.f + __builtin_amdgcn_exp2f(-g2.y));
;                         const f32x2 o2 = g2 * u2 * r2; hv[2 * q] = o2.x; hv[2 * q + 1] = o2.y; }
;                     if (n == 0) h0 = hv; else h1 = hv; }
;                 unsigned w0 = 0u, w1 = 0u;
;                 w0 = __builtin_amdgcn_cvt_pk_fp8_f32(h0[0], h0[1], w0, false); w0 = __builtin_amdgcn_cvt_pk_fp8_f32(h0[2], h0[3], w0, true); w1 = __builtin_amdgcn_cvt_pk_fp8_f32(h1[0], h1[1], w1, false); w1 = __builtin_amdgcn_cvt_pk_fp8_f32(h1[2], h1[3], w1, true);
;                 *(u32x2*)(hb + (ai * 4 + m) * 512) = (u32x2){w0, w1}; asm volatile("" ::: "memory"); }
	v_add_f32_e32 v68, v72, v73
	v_fmamk_f32 v68, v68, 0x3a800000, v227
	v_rsq_f32_e32 v69, v68
	v_mov_b32_e32 v212, v80
	v_mov_b32_e32 v213, v81
	s_nop 1
	v_permlane16_swap_b32_e32 v212, v214
	v_permlane16_swap_b32_e32 v213, v215
	global_store_dwordx4 v[216:217], v[212:215], off offset:1024
	v_mul_f32_e32 v68, 0x3fb8aa3b, v69
	v_pk_mul_f32 v[64:65], v[64:65], v[68:69] op_sel_hi:[1,0]
	v_mul_f32_e32 v70, 0x3f317218, v69
	v_exp_f32_e64 v71, -v64
	v_exp_f32_e64 v69, -v65
	v_pk_mul_f32 v[56:57], v[56:57], v[70:71] op_sel_hi:[1,0]
	v_add_f32_e32 v69, 1.0, v69
	v_pk_mul_f32 v[56:57], v[64:65], v[56:57]
	v_pk_mul_f32 v[64:65], v[66:67], v[68:69] op_sel_hi:[1,0]
	v_add_f32_e32 v71, 1.0, v71
	v_exp_f32_e64 v66, -v64
	v_exp_f32_e64 v67, -v65
	v_pk_mul_f32 v[58:59], v[58:59], v[70:71] op_sel_hi:[1,0]
	v_pk_mul_f32 v[60:61], v[60:61], v[68:69] op_sel_hi:[1,0]
	v_add_f32_e32 v66, 1.0, v66
	v_add_f32_e32 v67, 1.0, v67
	v_pk_mul_f32 v[58:59], v[64:65], v[58:59]
	v_exp_f32_e64 v64, -v60
	v_exp_f32_e64 v65, -v61
	v_rcp_f32_e32 v66, v66
	v_rcp_f32_e32 v67, v67
	v_add_f32_e32 v64, 1.0, v64
	v_add_f32_e32 v65, 1.0, v65
	v_pk_mul_f32 v[62:63], v[62:63], v[68:69] op_sel_hi:[1,0]
	v_pk_mul_f32 v[58:59], v[58:59], v[66:67]
	v_rcp_f32_e32 v64, v64
	v_rcp_f32_e32 v65, v65
	v_exp_f32_e64 v66, -v62
	v_pk_mul_f32 v[52:53], v[52:53], v[70:71] op_sel_hi:[1,0]
	v_rcp_f32_e32 v72, v71
	v_pk_mul_f32 v[52:53], v[60:61], v[52:53]
	s_waitcnt vmcnt(4)
	v_mov_b32_e32 v60, v141
	v_mov_b32_e32 v61, v142
	v_mov_b32_e32 v141, v143
	v_pk_add_f32 v[60:61], v[60:61], v[140:141]
	v_pk_mul_f32 v[52:53], v[52:53], v[64:65]
	v_add_f32_e32 v64, 1.0, v66
	v_add_f32_e32 v66, v60, v61
	ds_bpermute_b32 v67, v168, v66
	v_exp_f32_e64 v65, -v63
	v_rcp_f32_e32 v60, v64
	v_rcp_f32_e32 v73, v69
	v_pk_mul_f32 v[54:55], v[54:55], v[70:71] op_sel_hi:[1,0]
	s_waitcnt lgkmcnt(0)
	v_add_f32_e32 v64, v66, v67
	v_add_f32_e32 v61, 1.0, v65
	ds_bpermute_b32 v65, v167, v64
	v_pk_mul_f32 v[54:55], v[62:63], v[54:55]
	v_mov_b32_e32 v63, v3
	v_cvt_pk_fp8_f32 v63, v52, v53
	v_pk_mul_f32 v[56:57], v[56:57], v[72:73]
	s_waitcnt lgkmcnt(0)
	v_add_f32_e32 v52, v64, v65
	v_rcp_f32_e32 v61, v61
	v_mov_b32_e32 v62, v3
	v_fmamk_f32 v52, v52, 0x3a800000, v227
	v_cvt_pk_fp8_f32 v62, v56, v57
	v_rsq_f32_e32 v56, v52
	v_pk_mul_f32 v[52:53], v[54:55], v[60:61]
	v_cvt_pk_fp8_f32 v62, v58, v59 op_sel:[0,0,1]
	v_cvt_pk_fp8_f32 v63, v52, v53 op_sel:[0,0,1]
	v_mul_f32_e32 v52, 0x3fb8aa3b, v56
	v_pk_mul_f32 v[48:49], v[48:49], v[52:53] op_sel_hi:[1,0]
	v_mul_f32_e32 v54, 0x3f317218, v56
	v_exp_f32_e64 v53, -v48
	v_exp_f32_e64 v55, -v49
	v_mov_b32_e32 v210, v62
	v_mov_b32_e32 v211, v63
	v_add_f32_e32 v53, 1.0, v53
	v_pk_mul_f32 v[40:41], v[40:41], v[54:55] op_sel_hi:[1,0]
	v_rcp_f32_e32 v56, v53
	v_add_f32_e32 v53, 1.0, v55
	v_pk_mul_f32 v[40:41], v[48:49], v[40:41]
	v_pk_mul_f32 v[48:49], v[50:51], v[52:53] op_sel_hi:[1,0]
	v_pk_mul_f32 v[42:43], v[42:43], v[54:55] op_sel_hi:[1,0]
	v_pk_mul_f32 v[44:45], v[44:45], v[52:53] op_sel_hi:[1,0]
	v_exp_f32_e64 v50, -v48
	v_exp_f32_e64 v51, -v49
	v_pk_mul_f32 v[42:43], v[48:49], v[42:43]
	v_exp_f32_e64 v48, -v44
	v_exp_f32_e64 v49, -v45
	v_add_f32_e32 v50, 1.0, v50
	v_add_f32_e32 v51, 1.0, v51
	v_add_f32_e32 v48, 1.0, v48
	v_add_f32_e32 v49, 1.0, v49
	v_rcp_f32_e32 v48, v48
	v_rcp_f32_e32 v49, v49
	v_rcp_f32_e32 v50, v50
	v_rcp_f32_e32 v51, v51
	v_pk_mul_f32 v[36:37], v[36:37], v[54:55] op_sel_hi:[1,0]
	v_rcp_f32_e32 v57, v53
	v_pk_mul_f32 v[36:37], v[44:45], v[36:37]
	v_pk_mul_f32 v[42:43], v[42:43], v[50:51]
	v_pk_mul_f32 v[36:37], v[36:37], v[48:49]
	s_waitcnt vmcnt(3)
	v_mov_b32_e32 v48, v137
	v_mov_b32_e32 v49, v138
	v_mov_b32_e32 v137, v139
	v_pk_add_f32 v[48:49], v[48:49], v[136:137]
	v_pk_mul_f32 v[44:45], v[46:47], v[52:53] op_sel_hi:[1,0]
	v_add_f32_e32 v50, v48, v49
	ds_bpermute_b32 v51, v168, v50
	v_exp_f32_e64 v46, -v44
	v_exp_f32_e64 v47, -v45
	v_pk_mul_f32 v[40:41], v[40:41], v[56:57]
	v_mov_b32_e32 v48, v3
	v_add_f32_e32 v46, 1.0, v46
	v_add_f32_e32 v47, 1.0, v47
	v_cvt_pk_fp8_f32 v48, v40, v41
	s_waitcnt lgkmcnt(0)
	v_add_f32_e32 v40, v50, v51
	v_rcp_f32_e32 v46, v46
	v_rcp_f32_e32 v47, v47
	v_mov_b32_e32 v49, v3
	ds_bpermute_b32 v41, v167, v40
	v_cvt_pk_fp8_f32 v49, v36, v37
	v_pk_mul_f32 v[38:39], v[38:39], v[54:55] op_sel_hi:[1,0]
	v_cvt_pk_fp8_f32 v48, v42, v43 op_sel:[0,0,1]
	v_pk_mul_f32 v[36:37], v[44:45], v[38:39]
	s_nop 0
	v_pk_mul_f32 v[36:37], v[36:37], v[46:47]
	s_nop 0
	v_cvt_pk_fp8_f32 v49, v36, v37 op_sel:[0,0,1]
	s_waitcnt lgkmcnt(0)
; __device__ __forceinline__ float rstd_fin4(const f32x4 a) { float s = (a[0] + a[1]) + (a[2] + a[3]); s += __shfl_xor(s, 16); s += __shfl_xor(s, 32); return __builtin_amdgcn_rsqf(s * (1.f / 1024.f) + 1e-6f); }
;     __device__ __forceinline__ void operator()(const f32x4 (&acc)[2][2][4][2], const Unit& u, int wr, int wc, int fr, int fq) const {
;     ...
;             for (int m = 0; m < 4; ++m) { const float rs = rstd_fin4(pa[ai][m]) * sc;
;                 const float rsl = rs * 1.4426950408889634f, rsu = rs * 0.6931471805599453f;
;                 f32x4 h0, h1;
; #pragma unroll
;                 for (int n = 0; n < 2; ++n) { const f32x4 G = acc[ai][0][m][n], U = acc[ai][1][m][n]; f32x4 hv;
; #pragma unroll
;                     for (int q = 0; q < 2; ++q) { const f32x2 g2 = (f32x2){G[2 * q], G[2 * q + 1]} * rsl, u2 = (f32x2){U[2 * q], U[2 * q + 1]} * rsu;
;                         f32x2 r2; r2.x = __builtin_amdgcn_rcpf(1.f + __builtin_amdgcn_exp2f(-g2.x)); r2.y = __builtin_amdgcn_rcpf(1.f + __builtin_amdgcn_exp2f(-g2.y));
;                         const f32x2 o2 = g2 * u2 * r2; hv[2 * q] = o2.x; hv[2 * q + 1] = o2.y; }
;                     if (n == 0) h0 = hv; else h1 = hv; }
;                 unsigned w0 = 0u, w1 = 0u;
;                 w0 = __builtin_amdgcn_cvt_pk_fp8_f32(h0[0], h0[1], w0, false); w0 = __builtin_amdgcn_cvt_pk_fp8_f32(h0[2], h0[3], w0, true); w1 = __builtin_amdgcn_cvt_pk_fp8_f32(h1[0], h1[1], w1, false); w1 = __builtin_amdgcn_cvt_pk_fp8_f32(h1[2], h1[3], w1, true);
;                 *(u32x2*)(hb + (ai * 4 + m) * 512) = (u32x2){w0, w1}; asm volatile("" ::: "memory"); }
	v_add_f32_e32 v36, v40, v41
	v_fmamk_f32 v36, v36, 0x3a800000, v227
	v_rsq_f32_e32 v37, v36
	v_mov_b32_e32 v208, v48
	v_mov_b32_e32 v209, v49
	s_nop 1
	v_permlane16_swap_b32_e32 v208, v210
	v_permlane16_swap_b32_e32 v209, v211
	global_store_dwordx4 v[216:217], v[208:211], off offset:2048
	v_mul_f32_e32 v36, 0x3fb8aa3b, v37
	v_pk_mul_f32 v[32:33], v[32:33], v[36:37] op_sel_hi:[1,0]
	v_mul_f32_e32 v38, 0x3f317218, v37
	v_exp_f32_e64 v39, -v32
	v_exp_f32_e64 v37, -v33
	v_pk_mul_f32 v[24:25], v[24:25], v[38:39] op_sel_hi:[1,0]
	v_add_f32_e32 v37, 1.0, v37
	v_pk_mul_f32 v[24:25], v[32:33], v[24:25]
	v_pk_mul_f32 v[32:33], v[34:35], v[36:37] op_sel_hi:[1,0]
	v_add_f32_e32 v39, 1.0, v39
	v_exp_f32_e64 v34, -v32
	v_exp_f32_e64 v35, -v33
	v_pk_mul_f32 v[26:27], v[26:27], v[38:39] op_sel_hi:[1,0]
	v_pk_mul_f32 v[28:29], v[28:29], v[36:37] op_sel_hi:[1,0]
	v_add_f32_e32 v34, 1.0, v34
	v_add_f32_e32 v35, 1.0, v35
	v_pk_mul_f32 v[26:27], v[32:33], v[26:27]
	v_exp_f32_e64 v32, -v28
	v_exp_f32_e64 v33, -v29
	v_rcp_f32_e32 v34, v34
	v_rcp_f32_e32 v35, v35
	v_add_f32_e32 v32, 1.0, v32
	v_add_f32_e32 v33, 1.0, v33
	v_pk_mul_f32 v[30:31], v[30:31], v[36:37] op_sel_hi:[1,0]
	v_pk_mul_f32 v[26:27], v[26:27], v[34:35]
	v_rcp_f32_e32 v32, v32
	v_rcp_f32_e32 v33, v33
	v_exp_f32_e64 v34, -v30
	v_pk_mul_f32 v[20:21], v[20:21], v[38:39] op_sel_hi:[1,0]
	v_rcp_f32_e32 v40, v39
	v_pk_mul_f32 v[20:21], v[28:29], v[20:21]
	s_waitcnt vmcnt(3)
	v_mov_b32_e32 v28, v133
	v_mov_b32_e32 v29, v134
	v_mov_b32_e32 v133, v135
	v_pk_add_f32 v[28:29], v[28:29], v[132:133]
	v_pk_mul_f32 v[20:21], v[20:21], v[32:33]
	v_add_f32_e32 v32, 1.0, v34
	v_add_f32_e32 v34, v28, v29
	ds_bpermute_b32 v35, v168, v34
	v_exp_f32_e64 v33, -v31
	v_rcp_f32_e32 v28, v32
	v_rcp_f32_e32 v41, v37
	v_pk_mul_f32 v[22:23], v[22:23], v[38:39] op_sel_hi:[1,0]
	s_waitcnt lgkmcnt(0)
	v_add_f32_e32 v32, v34, v35
	v_add_f32_e32 v29, 1.0, v33
	ds_bpermute_b32 v33, v167, v32
	v_pk_mul_f32 v[22:23], v[30:31], v[22:23]
	v_mov_b32_e32 v31, v3
	v_cvt_pk_fp8_f32 v31, v20, v21
	v_pk_mul_f32 v[24:25], v[24:25], v[40:41]
	s_waitcnt lgkmcnt(0)
	v_add_f32_e32 v20, v32, v33
	v_rcp_f32_e32 v29, v29
	v_mov_b32_e32 v30, v3
	v_fmamk_f32 v20, v20, 0x3a800000, v227
	v_cvt_pk_fp8_f32 v30, v24, v25
	v_rsq_f32_e32 v24, v20
	v_pk_mul_f32 v[20:21], v[22:23], v[28:29]
	v_cvt_pk_fp8_f32 v30, v26, v27 op_sel:[0,0,1]
	v_cvt_pk_fp8_f32 v31, v20, v21 op_sel:[0,0,1]
	v_mul_f32_e32 v20, 0x3fb8aa3b, v24
	v_pk_mul_f32 v[16:17], v[16:17], v[20:21] op_sel_hi:[1,0]
	v_mul_f32_e32 v22, 0x3f317218, v24
	v_exp_f32_e64 v21, -v16
	v_exp_f32_e64 v23, -v17
	v_mov_b32_e32 v214, v30
	v_mov_b32_e32 v215, v31
	v_add_f32_e32 v21, 1.0, v21
	v_pk_mul_f32 v[8:9], v[8:9], v[22:23] op_sel_hi:[1,0]
	v_rcp_f32_e32 v24, v21
	v_add_f32_e32 v21, 1.0, v23
	v_pk_mul_f32 v[8:9], v[16:17], v[8:9]
	v_pk_mul_f32 v[16:17], v[18:19], v[20:21] op_sel_hi:[1,0]
	v_pk_mul_f32 v[10:11], v[10:11], v[22:23] op_sel_hi:[1,0]
	v_pk_mul_f32 v[12:13], v[12:13], v[20:21] op_sel_hi:[1,0]
	v_exp_f32_e64 v18, -v16
	v_exp_f32_e64 v19, -v17
	v_pk_mul_f32 v[10:11], v[16:17], v[10:11]
	v_exp_f32_e64 v16, -v12
	v_exp_f32_e64 v17, -v13
	v_pk_mul_f32 v[4:5], v[4:5], v[22:23] op_sel_hi:[1,0]
	v_rcp_f32_e32 v25, v21
	v_pk_mul_f32 v[4:5], v[12:13], v[4:5]
	v_pk_mul_f32 v[12:13], v[14:15], v[20:21] op_sel_hi:[1,0]
	v_add_f32_e32 v16, 1.0, v16
	v_add_f32_e32 v17, 1.0, v17
	v_exp_f32_e64 v14, -v12
	v_exp_f32_e64 v15, -v13
	v_rcp_f32_e32 v16, v16
	v_rcp_f32_e32 v17, v17
	v_add_f32_e32 v18, 1.0, v18
	v_add_f32_e32 v19, 1.0, v19
	v_add_f32_e32 v14, 1.0, v14
	v_add_f32_e32 v15, 1.0, v15
	v_pk_mul_f32 v[8:9], v[8:9], v[24:25]
	v_rcp_f32_e32 v18, v18
	v_rcp_f32_e32 v19, v19
	v_pk_mul_f32 v[4:5], v[4:5], v[16:17]
	v_rcp_f32_e32 v14, v14
	v_rcp_f32_e32 v15, v15
	v_mov_b32_e32 v16, v3
	v_mov_b32_e32 v17, v3
	v_cvt_pk_fp8_f32 v16, v8, v9
	v_cvt_pk_fp8_f32 v17, v4, v5
	v_pk_mul_f32 v[6:7], v[6:7], v[22:23] op_sel_hi:[1,0]
	v_pk_mul_f32 v[10:11], v[10:11], v[18:19]
	v_pk_mul_f32 v[4:5], v[12:13], v[6:7]
	v_cvt_pk_fp8_f32 v16, v10, v11 op_sel:[0,0,1]
	v_pk_mul_f32 v[4:5], v[4:5], v[14:15]
	s_nop 0
	v_cvt_pk_fp8_f32 v17, v4, v5 op_sel:[0,0,1]
	v_mov_b32_e32 v212, v16
	v_mov_b32_e32 v213, v17
	s_nop 1
	v_permlane16_swap_b32_e32 v212, v214
	v_permlane16_swap_b32_e32 v213, v215
	global_store_dwordx4 v[216:217], v[212:215], off offset:3072
	s_cbranch_vccnz .LBB0_427
	s_andn2_b64 vcc, exec, s[44:45]
	s_cbranch_vccnz .LBB0_426
	s_barrier
	s_branch .LBB0_426

; __device__ __forceinline__ float rstd_fin4(const f32x4 a) { float s = (a[0] + a[1]) + (a[2] + a[3]); s += __shfl_xor(s, 16); s += __shfl_xor(s, 32); return __builtin_amdgcn_rsqf(s * (1.f / 1024.f) + 1e-6f); }
;     __device__ __forceinline__ void operator()(const f32x4 (&acc)[2][2][4][2], const Unit& u, int wr, int wc, int fr, int fq) const {
;         asm volatile("" : "+v"(fr), "+v"(fq));
;         const int row0 = u.pm * BM + wr * 64 + fr;
;         unsigned char* const hb = (unsigned char*)H + (size_t)(u.pm * (FFH / 128) + u.pn + pn0) * 32768 + (((wr * 4 + wc) * 8) * 64 + (fq >> 1) * 32 + fr * 2 + (fq & 1)) * 8;
;         f32x4 pa[2][4];
; #pragma unroll
;         for (int ai = 0; ai < 2; ++ai)
; #pragma unroll
;             for (int m = 0; m < 4; ++m) pa[ai][m] = rstd_ld4(ss, row0 + ai * HALF + m * 16, fq);
; #pragma unroll
;         for (int ai = 0; ai < 2; ++ai)
; #pragma unroll
;             for (int m = 0; m < 4; ++m) { const float rs = rstd_fin4(pa[ai][m]) * sc;
;                 const float rsl = rs * 1.4426950408889634f, rsu = rs * 0.6931471805599453f;
;                 f32x4 h0, h1;
; #pragma unroll
;                 for (int n = 0; n < 2; ++n) { const f32x4 G = acc[ai][0][m][n], U = acc[ai][1][m][n]; f32x4 hv;
; #pragma unroll
;                     for (int q = 0; q < 2; ++q) { const f32x2 g2 = (f32x2){G[2 * q], G[2 * q + 1]} * rsl, u2 = (f32x2){U[2 * q], U[2 * q + 1]} * rsu;
;                         f32x2 r2; r2.x = __builtin_amdgcn_rcpf(1.f + __builtin_amdgcn_exp2f(-g2.x)); r2.y = __builtin_amdgcn_rcpf(1.f + __builtin_amdgcn_exp2f(-g2.y));
;                         const f32x2 o2 = g2 * u2 * r2; hv[2 * q] = o2.x; hv[2 * q + 1] = o2.y; }
;                     if (n == 0) h0 = hv; else h1 = hv; }
;                 unsigned w0 = 0u, w1 = 0u;
;                 w0 = __builtin_amdgcn_cvt_pk_fp8_f32(h0[0], h0[1], w0, false); w0 = __builtin_amdgcn_cvt_pk_fp8_f32(h0[2], h0[3], w0, true); w1 = __builtin_amdgcn_cvt_pk_fp8_f32(h1[0], h1[1], w1, false); w1 = __builtin_amdgcn_cvt_pk_fp8_f32(h1[2], h1[3], w1, true);
;                 *(u32x2*)(hb + (ai * 4 + m) * 512) = (u32x2){w0, w1}; asm volatile("" ::: "memory"); }
.LBB0_1674:
	s_lshl_b32 s4, s72, 8
	v_mov_b32_e32 v14, v1
	v_mov_b32_e32 v15, v182
	s_add_i32 s4, s4, s66
	v_and_b32_e32 v17, 64, v246
	v_add_u32_e32 v4, s4, v14
	v_lshlrev_b32_e32 v6, 2, v15
	v_ashrrev_i32_e32 v7, 31, v6
	v_ashrrev_i32_e32 v5, 31, v4
	v_lshl_add_u64 v[6:7], v[6:7], 2, s[44:45]
	v_lshlrev_b64 v[4:5], 6, v[4:5]
	v_lshl_add_u64 v[12:13], v[6:7], 0, v[4:5]
	global_load_dwordx4 v[4:7], v[12:13], off
	global_load_dwordx4 v[8:11], v[12:13], off offset:1024
	global_load_dwordx4 v[28:31], v[12:13], off offset:2048
	global_load_dwordx4 v[20:23], v[12:13], off offset:3072
	v_xor_b32_e32 v16, 16, v246
	v_add_u32_e32 v17, 64, v17
	v_xor_b32_e32 v18, 32, v246
	v_cmp_lt_i32_e32 vcc, v16, v17
	v_mov_b32_e32 v32, v3
	v_mov_b32_e32 v33, v3
	v_cndmask_b32_e32 v16, v246, v16, vcc
	v_cmp_lt_i32_e32 vcc, v18, v17
	v_lshlrev_b32_e32 v27, 2, v16
	s_mul_i32 s4, s72, 22
	v_cndmask_b32_e32 v17, v246, v18, vcc
	v_lshlrev_b32_e32 v26, 2, v17
	s_add_i32 s4, s4, s71
	s_ashr_i32 s5, s4, 31
	v_lshlrev_b32_e32 v19, 4, v15
	v_lshl_add_u32 v14, v14, 1, s69
	s_lshl_b64 s[4:5], s[4:5], 15
	v_and_b32_e32 v18, 0x1fffffe0, v19
	v_and_or_b32 v14, v15, 1, v14
	v_add_lshl_u32 v14, v14, v18, 3
	s_add_u32 s4, s6, s4
	v_ashrrev_i32_e32 v15, 31, v14
	s_addc_u32 s5, s7, s5
	v_lshl_add_u64 v[24:25], s[4:5], 0, v[14:15]
	s_mov_b64 s[4:5], -1
	s_waitcnt vmcnt(0)
	v_mov_b32_e32 v16, v5
	v_mov_b32_e32 v17, v6
	v_mov_b32_e32 v5, v7
	v_mov_b32_e32 v6, v9
	v_mov_b32_e32 v7, v10
	v_mov_b32_e32 v9, v11
	v_pk_add_f32 v[4:5], v[16:17], v[4:5]
	v_pk_add_f32 v[6:7], v[6:7], v[8:9]
	v_add_f32_e32 v8, v4, v5
	v_add_f32_e32 v6, v6, v7
	ds_bpermute_b32 v7, v27, v8
	ds_bpermute_b32 v9, v27, v6
	v_add_co_u32_e32 v4, vcc, s88, v12
	s_waitcnt lgkmcnt(1)
	v_add_f32_e32 v7, v8, v7
	s_waitcnt lgkmcnt(0)
	v_add_f32_e32 v6, v6, v9
	ds_bpermute_b32 v8, v26, v7
	ds_bpermute_b32 v9, v26, v6
	v_addc_co_u32_e32 v5, vcc, 0, v13, vcc
	global_load_dwordx4 v[16:19], v[4:5], off
	global_load_dwordx4 v[12:15], v[4:5], off offset:1024
	s_waitcnt lgkmcnt(1)
	v_add_f32_e32 v7, v7, v8
	s_waitcnt lgkmcnt(0)
	v_add_f32_e32 v6, v6, v9
	v_fmamk_f32 v7, v7, 0x3a800000, v227
	v_fmamk_f32 v6, v6, 0x3a800000, v227
	v_rsq_f32_e32 v34, v7
	v_rsq_f32_e32 v35, v6
	global_load_dwordx4 v[8:11], v[4:5], off offset:2048
	s_nop 0
	global_load_dwordx4 v[4:7], v[4:5], off offset:3072
	s_andn2_b64 vcc, exec, s[40:41]
	v_mul_f32_e32 v174, 0x3c800000, v34
	v_mul_f32_e32 v35, 0x3c800000, v35
	v_mul_f32_e32 v34, 0x3fb8aa3b, v174
	v_mul_f32_e32 v174, 0x3f317218, v174
	v_pk_mul_f32 v[160:161], v[160:161], v[34:35] op_sel_hi:[1,0]
	v_pk_mul_f32 v[152:153], v[152:153], v[174:175] op_sel_hi:[1,0]
	v_pk_mul_f32 v[162:163], v[162:163], v[34:35] op_sel_hi:[1,0]
	v_pk_mul_f32 v[154:155], v[154:155], v[174:175] op_sel_hi:[1,0]
	v_pk_mul_f32 v[156:157], v[156:157], v[34:35] op_sel_hi:[1,0]
	v_mul_f32_e32 v176, 0x3fb8aa3b, v35
	v_mul_f32_e32 v178, 0x3f317218, v35
	v_pk_mul_f32 v[148:149], v[148:149], v[174:175] op_sel_hi:[1,0]
	v_pk_mul_f32 v[34:35], v[158:159], v[34:35] op_sel_hi:[1,0]
	v_exp_f32_e64 v158, -v160
	v_exp_f32_e64 v159, -v161
	v_pk_mul_f32 v[152:153], v[160:161], v[152:153]
	v_exp_f32_e64 v160, -v162
	v_exp_f32_e64 v161, -v163
	v_pk_mul_f32 v[154:155], v[162:163], v[154:155]
	v_exp_f32_e64 v162, -v156
	v_exp_f32_e64 v163, -v157
	v_pk_mul_f32 v[148:149], v[156:157], v[148:149]
	v_exp_f32_e64 v156, -v34
	v_exp_f32_e64 v157, -v35
	v_pk_mul_f32 v[150:151], v[150:151], v[174:175] op_sel_hi:[1,0]
	v_pk_mul_f32 v[144:145], v[144:145], v[176:177] op_sel_hi:[1,0]
	v_pk_mul_f32 v[34:35], v[34:35], v[150:151]
	v_add_f32_e32 v150, 1.0, v158
	v_add_f32_e32 v151, 1.0, v159
	v_add_f32_e32 v158, 1.0, v160
	v_add_f32_e32 v159, 1.0, v161
	v_add_f32_e32 v160, 1.0, v162
	v_add_f32_e32 v161, 1.0, v163
	v_add_f32_e32 v162, 1.0, v156
	v_add_f32_e32 v163, 1.0, v157
	v_rcp_f32_e32 v150, v150
	v_rcp_f32_e32 v151, v151
	v_rcp_f32_e32 v156, v158
	v_rcp_f32_e32 v157, v159
	v_rcp_f32_e32 v158, v160
	v_rcp_f32_e32 v159, v161
	v_rcp_f32_e32 v160, v162
	v_rcp_f32_e32 v161, v163
	v_pk_mul_f32 v[150:151], v[152:153], v[150:151]
	v_pk_mul_f32 v[148:149], v[148:149], v[158:159]
	v_cvt_pk_fp8_f32 v32, v150, v151
	v_cvt_pk_fp8_f32 v33, v148, v149
	v_pk_mul_f32 v[148:149], v[154:155], v[156:157]
	v_pk_mul_f32 v[34:35], v[34:35], v[160:161]
	v_cvt_pk_fp8_f32 v32, v148, v149 op_sel:[0,0,1]
	v_cvt_pk_fp8_f32 v33, v34, v35 op_sel:[0,0,1]
	v_exp_f32_e64 v35, -v145
	v_exp_f32_e64 v174, -v144
	v_pk_mul_f32 v[136:137], v[136:137], v[178:179] op_sel_hi:[1,0]
	v_and_b32_e32 v218, 16, v246
	v_mov_b32_e32 v219, 0x200
	v_cmp_eq_u32_e64 s[60:61], 0, v218
	s_nop 1
	v_cndmask_b32_e64 v218, -8, v219, s[60:61]
	v_ashrrev_i32_e32 v219, 31, v218
	v_lshl_add_u64 v[216:217], v[24:25], 0, v[218:219]
	v_mov_b32_e32 v210, v32
	v_mov_b32_e32 v211, v33
	v_add_f32_e32 v32, 1.0, v35
	v_add_f32_e32 v34, 1.0, v174
	v_rcp_f32_e32 v35, v32
	v_pk_mul_f32 v[32:33], v[144:145], v[136:137]
	v_pk_mul_f32 v[136:137], v[146:147], v[176:177] op_sel_hi:[1,0]
	v_rcp_f32_e32 v34, v34
	v_exp_f32_e64 v144, -v136
	v_exp_f32_e64 v145, -v137
	v_pk_mul_f32 v[132:133], v[132:133], v[178:179] op_sel_hi:[1,0]
	v_pk_mul_f32 v[32:33], v[32:33], v[34:35]
	v_pk_mul_f32 v[34:35], v[138:139], v[178:179] op_sel_hi:[1,0]
	v_add_f32_e32 v138, 1.0, v144
	v_add_f32_e32 v139, 1.0, v145
	v_rcp_f32_e32 v138, v138
	v_rcp_f32_e32 v139, v139
	v_pk_mul_f32 v[34:35], v[136:137], v[34:35]
	v_pk_mul_f32 v[136:137], v[140:141], v[176:177] op_sel_hi:[1,0]
	v_pk_mul_f32 v[134:135], v[134:135], v[178:179] op_sel_hi:[1,0]
	v_exp_f32_e64 v140, -v136
	v_pk_mul_f32 v[34:35], v[34:35], v[138:139]
	v_exp_f32_e64 v139, -v137
	v_pk_mul_f32 v[132:133], v[136:137], v[132:133]
	v_mov_b32_e32 v136, v29
	v_mov_b32_e32 v137, v30
	v_mov_b32_e32 v29, v31
	v_pk_add_f32 v[28:29], v[136:137], v[28:29]
	v_add_f32_e32 v138, 1.0, v140
	v_add_f32_e32 v136, v28, v29
	ds_bpermute_b32 v137, v27, v136
	v_add_f32_e32 v139, 1.0, v139
	v_rcp_f32_e32 v138, v138
	v_rcp_f32_e32 v139, v139
	v_pk_mul_f32 v[140:141], v[142:143], v[176:177] op_sel_hi:[1,0]
	s_waitcnt lgkmcnt(0)
; __device__ __forceinline__ float rstd_fin4(const f32x4 a) { float s = (a[0] + a[1]) + (a[2] + a[3]); s += __shfl_xor(s, 16); s += __shfl_xor(s, 32); return __builtin_amdgcn_rsqf(s * (1.f / 1024.f) + 1e-6f); }
;     __device__ __forceinline__ void operator()(const f32x4 (&acc)[2][2][4][2], const Unit& u, int wr, int wc, int fr, int fq) const {
;     ...
;             for (int m = 0; m < 4; ++m) { const float rs = rstd_fin4(pa[ai][m]) * sc;
;                 const float rsl = rs * 1.4426950408889634f, rsu = rs * 0.6931471805599453f;
;                 f32x4 h0, h1;
; #pragma unroll
;                 for (int n = 0; n < 2; ++n) { const f32x4 G = acc[ai][0][m][n], U = acc[ai][1][m][n]; f32x4 hv;
; #pragma unroll
;                     for (int q = 0; q < 2; ++q) { const f32x2 g2 = (f32x2){G[2 * q], G[2 * q + 1]} * rsl, u2 = (f32x2){U[2 * q], U[2 * q + 1]} * rsu;
;                         f32x2 r2; r2.x = __builtin_amdgcn_rcpf(1.f + __builtin_amdgcn_exp2f(-g2.x)); r2.y = __builtin_amdgcn_rcpf(1.f + __builtin_amdgcn_exp2f(-g2.y));
;                         const f32x2 o2 = g2 * u2 * r2; hv[2 * q] = o2.x; hv[2 * q + 1] = o2.y; }
;                     if (n == 0) h0 = hv; else h1 = hv; }
;                 unsigned w0 = 0u, w1 = 0u;
;                 w0 = __builtin_amdgcn_cvt_pk_fp8_f32(h0[0], h0[1], w0, false); w0 = __builtin_amdgcn_cvt_pk_fp8_f32(h0[2], h0[3], w0, true); w1 = __builtin_amdgcn_cvt_pk_fp8_f32(h1[0], h1[1], w1, false); w1 = __builtin_amdgcn_cvt_pk_fp8_f32(h1[2], h1[3], w1, true);
;                 *(u32x2*)(hb + (ai * 4 + m) * 512) = (u32x2){w0, w1}; asm volatile("" ::: "memory"); }
	v_add_f32_e32 v136, v136, v137
	ds_bpermute_b32 v137, v26, v136
	v_exp_f32_e64 v142, -v140
	v_pk_mul_f32 v[132:133], v[132:133], v[138:139]
	v_exp_f32_e64 v139, -v141
	v_pk_mul_f32 v[30:31], v[140:141], v[134:135]
	v_mov_b32_e32 v134, v3
	v_add_f32_e32 v138, 1.0, v142
	v_add_f32_e32 v29, 1.0, v139
	v_cvt_pk_fp8_f32 v134, v32, v33
	s_waitcnt lgkmcnt(0)
	v_add_f32_e32 v32, v136, v137
	v_rcp_f32_e32 v28, v138
	v_rcp_f32_e32 v29, v29
	v_mov_b32_e32 v135, v3
	v_fmamk_f32 v32, v32, 0x3a800000, v227
	v_cvt_pk_fp8_f32 v135, v132, v133
	v_rsq_f32_e32 v32, v32
	v_pk_mul_f32 v[28:29], v[30:31], v[28:29]
	v_cvt_pk_fp8_f32 v134, v34, v35 op_sel:[0,0,1]
	v_cvt_pk_fp8_f32 v135, v28, v29 op_sel:[0,0,1]
	v_mul_f32_e32 v29, 0x3c800000, v32
	v_mul_f32_e32 v28, 0x3fb8aa3b, v29
	v_pk_mul_f32 v[30:31], v[128:129], v[28:29] op_sel_hi:[1,0]
	v_mul_f32_e32 v32, 0x3f317218, v29
	v_exp_f32_e64 v33, -v30
	v_exp_f32_e64 v29, -v31
	v_mov_b32_e32 v208, v134
	v_mov_b32_e32 v209, v135
	s_nop 1
	v_permlane16_swap_b32_e32 v208, v210
	v_permlane16_swap_b32_e32 v209, v211
	global_store_dwordx4 v[216:217], v[208:211], off
	v_pk_mul_f32 v[34:35], v[120:121], v[32:33] op_sel_hi:[1,0]
	v_add_f32_e32 v29, 1.0, v29
	v_pk_mul_f32 v[30:31], v[30:31], v[34:35]
	v_pk_mul_f32 v[34:35], v[130:131], v[28:29] op_sel_hi:[1,0]
	v_add_f32_e32 v33, 1.0, v33
	v_rcp_f32_e32 v121, v29
	v_exp_f32_e64 v29, -v34
	v_rcp_f32_e32 v120, v33
	v_exp_f32_e64 v33, -v35
	v_add_f32_e32 v29, 1.0, v29
	v_pk_mul_f32 v[30:31], v[30:31], v[120:121]
	v_pk_mul_f32 v[120:121], v[122:123], v[32:33] op_sel_hi:[1,0]
	v_rcp_f32_e32 v122, v29
	v_add_f32_e32 v29, 1.0, v33
	v_pk_mul_f32 v[34:35], v[34:35], v[120:121]
	v_pk_mul_f32 v[120:121], v[124:125], v[28:29] op_sel_hi:[1,0]
	v_rcp_f32_e32 v123, v29
	v_exp_f32_e64 v29, -v120
	v_exp_f32_e64 v33, -v121
	v_pk_mul_f32 v[34:35], v[34:35], v[122:123]
	v_add_f32_e32 v29, 1.0, v29
	v_rcp_f32_e32 v122, v29
	v_add_f32_e32 v29, 1.0, v33
	v_pk_mul_f32 v[116:117], v[116:117], v[32:33] op_sel_hi:[1,0]
	v_rcp_f32_e32 v123, v29
	v_pk_mul_f32 v[28:29], v[126:127], v[28:29] op_sel_hi:[1,0]
	v_pk_mul_f32 v[116:117], v[120:121], v[116:117]
	v_exp_f32_e64 v120, -v28
	v_exp_f32_e64 v121, -v29
	v_pk_mul_f32 v[32:33], v[118:119], v[32:33] op_sel_hi:[1,0]
	v_pk_mul_f32 v[116:117], v[116:117], v[122:123]
	v_add_f32_e32 v118, 1.0, v120
	v_add_f32_e32 v119, 1.0, v121
	v_mov_b32_e32 v120, v21
	v_mov_b32_e32 v121, v22
	v_mov_b32_e32 v21, v23
	v_pk_add_f32 v[20:21], v[120:121], v[20:21]
	v_rcp_f32_e32 v118, v118
	v_add_f32_e32 v22, v20, v21
	ds_bpermute_b32 v23, v27, v22
	v_mov_b32_e32 v20, v3
	v_cvt_pk_fp8_f32 v20, v30, v31
	v_rcp_f32_e32 v119, v119
	v_mov_b32_e32 v21, v3
	s_waitcnt lgkmcnt(0)
	v_add_f32_e32 v30, v22, v23
	ds_bpermute_b32 v31, v26, v30
	v_cvt_pk_fp8_f32 v21, v116, v117
	v_pk_mul_f32 v[22:23], v[28:29], v[32:33]
	v_cvt_pk_fp8_f32 v20, v34, v35 op_sel:[0,0,1]
	v_pk_mul_f32 v[22:23], v[22:23], v[118:119]
	s_nop 0
	v_cvt_pk_fp8_f32 v21, v22, v23 op_sel:[0,0,1]
	s_waitcnt lgkmcnt(0)
	v_add_f32_e32 v22, v30, v31
	v_fmamk_f32 v22, v22, 0x3a800000, v227
	v_rsq_f32_e32 v22, v22
	v_mov_b32_e32 v214, v20
	v_mov_b32_e32 v215, v21
	v_mul_f32_e32 v21, 0x3c800000, v22
	v_mul_f32_e32 v20, 0x3fb8aa3b, v21
	v_pk_mul_f32 v[22:23], v[112:113], v[20:21] op_sel_hi:[1,0]
	v_mul_f32_e32 v28, 0x3f317218, v21
	v_exp_f32_e64 v29, -v22
	v_exp_f32_e64 v21, -v23
	v_pk_mul_f32 v[30:31], v[104:105], v[28:29] op_sel_hi:[1,0]
	v_add_f32_e32 v21, 1.0, v21
	v_pk_mul_f32 v[22:23], v[22:23], v[30:31]
	v_pk_mul_f32 v[30:31], v[114:115], v[20:21] op_sel_hi:[1,0]
	v_add_f32_e32 v29, 1.0, v29
	v_rcp_f32_e32 v33, v21
	v_exp_f32_e64 v21, -v30
	v_rcp_f32_e32 v32, v29
	v_exp_f32_e64 v29, -v31
	v_add_f32_e32 v21, 1.0, v21
	v_pk_mul_f32 v[22:23], v[22:23], v[32:33]
	v_pk_mul_f32 v[32:33], v[106:107], v[28:29] op_sel_hi:[1,0]
	v_rcp_f32_e32 v34, v21
	v_add_f32_e32 v21, 1.0, v29
	v_pk_mul_f32 v[30:31], v[30:31], v[32:33]
	v_pk_mul_f32 v[32:33], v[108:109], v[20:21] op_sel_hi:[1,0]
	v_rcp_f32_e32 v35, v21
	v_exp_f32_e64 v21, -v32
	v_exp_f32_e64 v29, -v33
	v_pk_mul_f32 v[30:31], v[30:31], v[34:35]
	v_add_f32_e32 v21, 1.0, v21
	v_pk_mul_f32 v[34:35], v[100:101], v[28:29] op_sel_hi:[1,0]
	v_rcp_f32_e32 v100, v21
	v_add_f32_e32 v21, 1.0, v29
	v_rcp_f32_e32 v101, v21
	v_pk_mul_f32 v[32:33], v[32:33], v[34:35]
	v_pk_mul_f32 v[20:21], v[110:111], v[20:21] op_sel_hi:[1,0]
	v_pk_mul_f32 v[28:29], v[102:103], v[28:29] op_sel_hi:[1,0]
	v_pk_mul_f32 v[32:33], v[32:33], v[100:101]
	s_waitcnt vmcnt(4)
	v_mov_b32_e32 v100, v17
	v_mov_b32_e32 v101, v18
	v_mov_b32_e32 v17, v19
	v_pk_add_f32 v[16:17], v[100:101], v[16:17]
	v_exp_f32_e64 v34, -v20
	v_add_f32_e32 v18, v16, v17
	ds_bpermute_b32 v19, v27, v18
	v_exp_f32_e64 v35, -v21
	v_mov_b32_e32 v16, v3
	v_add_f32_e32 v34, 1.0, v34
	v_cvt_pk_fp8_f32 v16, v22, v23
	v_add_f32_e32 v35, 1.0, v35
	s_waitcnt lgkmcnt(0)
	v_add_f32_e32 v22, v18, v19
	v_rcp_f32_e32 v34, v34
	v_rcp_f32_e32 v35, v35
	v_mov_b32_e32 v17, v3
	ds_bpermute_b32 v23, v26, v22
	v_cvt_pk_fp8_f32 v17, v32, v33
	v_pk_mul_f32 v[18:19], v[20:21], v[28:29]
	v_cvt_pk_fp8_f32 v16, v30, v31 op_sel:[0,0,1]
	v_pk_mul_f32 v[18:19], v[18:19], v[34:35]
	s_nop 0
	v_cvt_pk_fp8_f32 v17, v18, v19 op_sel:[0,0,1]
	s_waitcnt lgkmcnt(0)
; __device__ __forceinline__ float rstd_fin4(const f32x4 a) { float s = (a[0] + a[1]) + (a[2] + a[3]); s += __shfl_xor(s, 16); s += __shfl_xor(s, 32); return __builtin_amdgcn_rsqf(s * (1.f / 1024.f) + 1e-6f); }
;     __device__ __forceinline__ void operator()(const f32x4 (&acc)[2][2][4][2], const Unit& u, int wr, int wc, int fr, int fq) const {
;     ...
;             for (int m = 0; m < 4; ++m) { const float rs = rstd_fin4(pa[ai][m]) * sc;
;                 const float rsl = rs * 1.4426950408889634f, rsu = rs * 0.6931471805599453f;
;                 f32x4 h0, h1;
; #pragma unroll
;                 for (int n = 0; n < 2; ++n) { const f32x4 G = acc[ai][0][m][n], U = acc[ai][1][m][n]; f32x4 hv;
; #pragma unroll
;                     for (int q = 0; q < 2; ++q) { const f32x2 g2 = (f32x2){G[2 * q], G[2 * q + 1]} * rsl, u2 = (f32x2){U[2 * q], U[2 * q + 1]} * rsu;
;                         f32x2 r2; r2.x = __builtin_amdgcn_rcpf(1.f + __builtin_amdgcn_exp2f(-g2.x)); r2.y = __builtin_amdgcn_rcpf(1.f + __builtin_amdgcn_exp2f(-g2.y));
;                         const f32x2 o2 = g2 * u2 * r2; hv[2 * q] = o2.x; hv[2 * q + 1] = o2.y; }
;                     if (n == 0) h0 = hv; else h1 = hv; }
;                 unsigned w0 = 0u, w1 = 0u;
;                 w0 = __builtin_amdgcn_cvt_pk_fp8_f32(h0[0], h0[1], w0, false); w0 = __builtin_amdgcn_cvt_pk_fp8_f32(h0[2], h0[3], w0, true); w1 = __builtin_amdgcn_cvt_pk_fp8_f32(h1[0], h1[1], w1, false); w1 = __builtin_amdgcn_cvt_pk_fp8_f32(h1[2], h1[3], w1, true);
;                 *(u32x2*)(hb + (ai * 4 + m) * 512) = (u32x2){w0, w1}; asm volatile("" ::: "memory"); }
	v_add_f32_e32 v18, v22, v23
	v_fmamk_f32 v18, v18, 0x3a800000, v227
	v_rsq_f32_e32 v18, v18
	v_mov_b32_e32 v212, v16
	v_mov_b32_e32 v213, v17
	s_nop 1
	v_permlane16_swap_b32_e32 v212, v214
	v_permlane16_swap_b32_e32 v213, v215
	global_store_dwordx4 v[216:217], v[212:215], off offset:1024
	v_mul_f32_e32 v17, 0x3c800000, v18
	v_mul_f32_e32 v16, 0x3fb8aa3b, v17
	v_pk_mul_f32 v[18:19], v[96:97], v[16:17] op_sel_hi:[1,0]
	v_mul_f32_e32 v20, 0x3f317218, v17
	v_exp_f32_e64 v21, -v18
	v_exp_f32_e64 v17, -v19
	v_pk_mul_f32 v[22:23], v[88:89], v[20:21] op_sel_hi:[1,0]
	v_add_f32_e32 v17, 1.0, v17
	v_pk_mul_f32 v[18:19], v[18:19], v[22:23]
	v_pk_mul_f32 v[22:23], v[98:99], v[16:17] op_sel_hi:[1,0]
	v_add_f32_e32 v21, 1.0, v21
	v_rcp_f32_e32 v29, v17
	v_exp_f32_e64 v17, -v22
	v_rcp_f32_e32 v28, v21
	v_exp_f32_e64 v21, -v23
	v_add_f32_e32 v17, 1.0, v17
	v_pk_mul_f32 v[18:19], v[18:19], v[28:29]
	v_pk_mul_f32 v[28:29], v[90:91], v[20:21] op_sel_hi:[1,0]
	v_rcp_f32_e32 v30, v17
	v_add_f32_e32 v17, 1.0, v21
	v_pk_mul_f32 v[22:23], v[22:23], v[28:29]
	v_pk_mul_f32 v[28:29], v[92:93], v[16:17] op_sel_hi:[1,0]
	v_rcp_f32_e32 v31, v17
	v_exp_f32_e64 v21, -v29
	v_exp_f32_e64 v17, -v28
	v_pk_mul_f32 v[22:23], v[22:23], v[30:31]
	v_pk_mul_f32 v[30:31], v[84:85], v[20:21] op_sel_hi:[1,0]
	v_add_f32_e32 v17, 1.0, v17
	v_pk_mul_f32 v[28:29], v[28:29], v[30:31]
	s_waitcnt vmcnt(4)
	v_mov_b32_e32 v30, v13
	v_mov_b32_e32 v31, v14
	v_mov_b32_e32 v13, v15
	v_pk_add_f32 v[12:13], v[30:31], v[12:13]
	v_rcp_f32_e32 v32, v17
	v_add_f32_e32 v30, v12, v13
	ds_bpermute_b32 v31, v27, v30
	v_add_f32_e32 v17, 1.0, v21
	v_rcp_f32_e32 v33, v17
	v_pk_mul_f32 v[16:17], v[94:95], v[16:17] op_sel_hi:[1,0]
	v_pk_mul_f32 v[20:21], v[86:87], v[20:21] op_sel_hi:[1,0]
	v_exp_f32_e64 v34, -v16
	v_pk_mul_f32 v[14:15], v[16:17], v[20:21]
	s_waitcnt lgkmcnt(0)
	v_add_f32_e32 v20, v30, v31
	ds_bpermute_b32 v21, v26, v20
	v_pk_mul_f32 v[28:29], v[28:29], v[32:33]
	v_exp_f32_e64 v33, -v17
	v_mov_b32_e32 v16, v3
	v_add_f32_e32 v32, 1.0, v34
	v_cvt_pk_fp8_f32 v16, v18, v19
	v_add_f32_e32 v13, 1.0, v33
	s_waitcnt lgkmcnt(0)
	v_add_f32_e32 v18, v20, v21
	v_rcp_f32_e32 v12, v32
	v_rcp_f32_e32 v13, v13
	v_mov_b32_e32 v17, v3
	v_fmamk_f32 v18, v18, 0x3a800000, v227
	v_cvt_pk_fp8_f32 v17, v28, v29
	v_rsq_f32_e32 v18, v18
	v_pk_mul_f32 v[12:13], v[14:15], v[12:13]
	v_cvt_pk_fp8_f32 v16, v22, v23 op_sel:[0,0,1]
	v_cvt_pk_fp8_f32 v17, v12, v13 op_sel:[0,0,1]
	v_mul_f32_e32 v13, 0x3c800000, v18
	v_mul_f32_e32 v12, 0x3fb8aa3b, v13
	v_pk_mul_f32 v[14:15], v[80:81], v[12:13] op_sel_hi:[1,0]
	v_mul_f32_e32 v18, 0x3f317218, v13
	v_exp_f32_e64 v19, -v14
	v_exp_f32_e64 v13, -v15
	v_mov_b32_e32 v210, v16
	v_mov_b32_e32 v211, v17
	v_pk_mul_f32 v[20:21], v[72:73], v[18:19] op_sel_hi:[1,0]
	v_add_f32_e32 v13, 1.0, v13
	v_pk_mul_f32 v[14:15], v[14:15], v[20:21]
	v_pk_mul_f32 v[20:21], v[82:83], v[12:13] op_sel_hi:[1,0]
	v_add_f32_e32 v19, 1.0, v19
	v_rcp_f32_e32 v23, v13
	v_exp_f32_e64 v13, -v20
	v_rcp_f32_e32 v22, v19
	v_exp_f32_e64 v19, -v21
	v_add_f32_e32 v13, 1.0, v13
	v_pk_mul_f32 v[14:15], v[14:15], v[22:23]
	v_pk_mul_f32 v[22:23], v[74:75], v[18:19] op_sel_hi:[1,0]
	v_rcp_f32_e32 v28, v13
	v_add_f32_e32 v13, 1.0, v19
	v_pk_mul_f32 v[20:21], v[20:21], v[22:23]
	v_pk_mul_f32 v[22:23], v[76:77], v[12:13] op_sel_hi:[1,0]
	v_rcp_f32_e32 v29, v13
	v_exp_f32_e64 v13, -v22
	v_exp_f32_e64 v19, -v23
	v_pk_mul_f32 v[20:21], v[20:21], v[28:29]
	v_add_f32_e32 v13, 1.0, v13
	v_rcp_f32_e32 v30, v13
	v_add_f32_e32 v13, 1.0, v19
	v_rcp_f32_e32 v31, v13
	v_pk_mul_f32 v[28:29], v[68:69], v[18:19] op_sel_hi:[1,0]
	v_pk_mul_f32 v[12:13], v[78:79], v[12:13] op_sel_hi:[1,0]
	v_pk_mul_f32 v[22:23], v[22:23], v[28:29]
	v_exp_f32_e64 v28, -v12
	v_pk_mul_f32 v[22:23], v[22:23], v[30:31]
	s_waitcnt vmcnt(3)
	v_mov_b32_e32 v30, v9
	v_mov_b32_e32 v31, v10
	v_mov_b32_e32 v9, v11
	v_pk_add_f32 v[8:9], v[30:31], v[8:9]
	v_exp_f32_e64 v29, -v13
	v_add_f32_e32 v10, v8, v9
	ds_bpermute_b32 v11, v27, v10
	v_mov_b32_e32 v8, v3
	v_add_f32_e32 v28, 1.0, v28
	v_add_f32_e32 v29, 1.0, v29
	v_cvt_pk_fp8_f32 v8, v14, v15
	s_waitcnt lgkmcnt(0)
	v_add_f32_e32 v14, v10, v11
	v_rcp_f32_e32 v28, v28
	v_rcp_f32_e32 v29, v29
	v_mov_b32_e32 v9, v3
	ds_bpermute_b32 v15, v26, v14
	v_cvt_pk_fp8_f32 v9, v22, v23
	v_pk_mul_f32 v[18:19], v[70:71], v[18:19] op_sel_hi:[1,0]
	v_cvt_pk_fp8_f32 v8, v20, v21 op_sel:[0,0,1]
	v_pk_mul_f32 v[10:11], v[12:13], v[18:19]
	s_nop 0
	v_pk_mul_f32 v[10:11], v[10:11], v[28:29]
	s_nop 0
	v_cvt_pk_fp8_f32 v9, v10, v11 op_sel:[0,0,1]
	s_waitcnt lgkmcnt(0)
; __device__ __forceinline__ float rstd_fin4(const f32x4 a) { float s = (a[0] + a[1]) + (a[2] + a[3]); s += __shfl_xor(s, 16); s += __shfl_xor(s, 32); return __builtin_amdgcn_rsqf(s * (1.f / 1024.f) + 1e-6f); }
;     __device__ __forceinline__ void operator()(const f32x4 (&acc)[2][2][4][2], const Unit& u, int wr, int wc, int fr, int fq) const {
;     ...
;             for (int m = 0; m < 4; ++m) { const float rs = rstd_fin4(pa[ai][m]) * sc;
;                 const float rsl = rs * 1.4426950408889634f, rsu = rs * 0.6931471805599453f;
;                 f32x4 h0, h1;
; #pragma unroll
;                 for (int n = 0; n < 2; ++n) { const f32x4 G = acc[ai][0][m][n], U = acc[ai][1][m][n]; f32x4 hv;
; #pragma unroll
;                     for (int q = 0; q < 2; ++q) { const f32x2 g2 = (f32x2){G[2 * q], G[2 * q + 1]} * rsl, u2 = (f32x2){U[2 * q], U[2 * q + 1]} * rsu;
;                         f32x2 r2; r2.x = __builtin_amdgcn_rcpf(1.f + __builtin_amdgcn_exp2f(-g2.x)); r2.y = __builtin_amdgcn_rcpf(1.f + __builtin_amdgcn_exp2f(-g2.y));
;                         const f32x2 o2 = g2 * u2 * r2; hv[2 * q] = o2.x; hv[2 * q + 1] = o2.y; }
;                     if (n == 0) h0 = hv; else h1 = hv; }
;                 unsigned w0 = 0u, w1 = 0u;
;                 w0 = __builtin_amdgcn_cvt_pk_fp8_f32(h0[0], h0[1], w0, false); w0 = __builtin_amdgcn_cvt_pk_fp8_f32(h0[2], h0[3], w0, true); w1 = __builtin_amdgcn_cvt_pk_fp8_f32(h1[0], h1[1], w1, false); w1 = __builtin_amdgcn_cvt_pk_fp8_f32(h1[2], h1[3], w1, true);
;                 *(u32x2*)(hb + (ai * 4 + m) * 512) = (u32x2){w0, w1}; asm volatile("" ::: "memory"); }
	v_add_f32_e32 v10, v14, v15
	v_fmamk_f32 v10, v10, 0x3a800000, v227
	v_rsq_f32_e32 v10, v10
	v_mov_b32_e32 v208, v8
	v_mov_b32_e32 v209, v9
	s_nop 1
	v_permlane16_swap_b32_e32 v208, v210
	v_permlane16_swap_b32_e32 v209, v211
	global_store_dwordx4 v[216:217], v[208:211], off offset:2048
	v_mul_f32_e32 v9, 0x3c800000, v10
	v_mul_f32_e32 v8, 0x3fb8aa3b, v9
	v_pk_mul_f32 v[10:11], v[64:65], v[8:9] op_sel_hi:[1,0]
	v_mul_f32_e32 v12, 0x3f317218, v9
	v_exp_f32_e64 v13, -v10
	v_exp_f32_e64 v9, -v11
	v_pk_mul_f32 v[14:15], v[56:57], v[12:13] op_sel_hi:[1,0]
	v_add_f32_e32 v9, 1.0, v9
	v_pk_mul_f32 v[10:11], v[10:11], v[14:15]
	v_pk_mul_f32 v[14:15], v[66:67], v[8:9] op_sel_hi:[1,0]
	v_add_f32_e32 v13, 1.0, v13
	v_rcp_f32_e32 v17, v9
	v_exp_f32_e64 v9, -v14
	v_rcp_f32_e32 v16, v13
	v_exp_f32_e64 v13, -v15
	v_add_f32_e32 v9, 1.0, v9
	v_pk_mul_f32 v[10:11], v[10:11], v[16:17]
	v_pk_mul_f32 v[16:17], v[58:59], v[12:13] op_sel_hi:[1,0]
	v_rcp_f32_e32 v18, v9
	v_add_f32_e32 v9, 1.0, v13
	v_pk_mul_f32 v[14:15], v[14:15], v[16:17]
	v_pk_mul_f32 v[16:17], v[60:61], v[8:9] op_sel_hi:[1,0]
	v_rcp_f32_e32 v19, v9
	v_exp_f32_e64 v13, -v17
	v_exp_f32_e64 v9, -v16
	v_pk_mul_f32 v[14:15], v[14:15], v[18:19]
	v_pk_mul_f32 v[18:19], v[52:53], v[12:13] op_sel_hi:[1,0]
	v_add_f32_e32 v9, 1.0, v9
	v_pk_mul_f32 v[16:17], v[16:17], v[18:19]
	s_waitcnt vmcnt(3)
	v_mov_b32_e32 v18, v5
	v_mov_b32_e32 v19, v6
	v_mov_b32_e32 v5, v7
	v_pk_add_f32 v[4:5], v[18:19], v[4:5]
	v_rcp_f32_e32 v20, v9
	v_add_f32_e32 v18, v4, v5
	ds_bpermute_b32 v19, v27, v18
	v_add_f32_e32 v9, 1.0, v13
	v_rcp_f32_e32 v21, v9
	v_pk_mul_f32 v[8:9], v[62:63], v[8:9] op_sel_hi:[1,0]
	v_pk_mul_f32 v[12:13], v[54:55], v[12:13] op_sel_hi:[1,0]
	v_exp_f32_e64 v22, -v8
	v_pk_mul_f32 v[6:7], v[8:9], v[12:13]
	s_waitcnt lgkmcnt(0)
	v_add_f32_e32 v12, v18, v19
	ds_bpermute_b32 v13, v26, v12
	v_pk_mul_f32 v[16:17], v[16:17], v[20:21]
	v_exp_f32_e64 v21, -v9
	v_mov_b32_e32 v8, v3
	v_add_f32_e32 v20, 1.0, v22
	v_cvt_pk_fp8_f32 v8, v10, v11
	v_add_f32_e32 v5, 1.0, v21
	s_waitcnt lgkmcnt(0)
	v_add_f32_e32 v10, v12, v13
	v_rcp_f32_e32 v4, v20
	v_rcp_f32_e32 v5, v5
	v_mov_b32_e32 v9, v3
	v_fmamk_f32 v10, v10, 0x3a800000, v227
	v_cvt_pk_fp8_f32 v9, v16, v17
	v_rsq_f32_e32 v10, v10
	v_pk_mul_f32 v[4:5], v[6:7], v[4:5]
	v_cvt_pk_fp8_f32 v8, v14, v15 op_sel:[0,0,1]
	v_cvt_pk_fp8_f32 v9, v4, v5 op_sel:[0,0,1]
	v_mul_f32_e32 v5, 0x3c800000, v10
	v_mul_f32_e32 v4, 0x3fb8aa3b, v5
	v_pk_mul_f32 v[6:7], v[48:49], v[4:5] op_sel_hi:[1,0]
	v_mul_f32_e32 v10, 0x3f317218, v5
	v_exp_f32_e64 v11, -v6
	v_exp_f32_e64 v5, -v7
	v_mov_b32_e32 v214, v8
	v_mov_b32_e32 v215, v9
	v_pk_mul_f32 v[12:13], v[40:41], v[10:11] op_sel_hi:[1,0]
	v_add_f32_e32 v5, 1.0, v5
	v_pk_mul_f32 v[6:7], v[6:7], v[12:13]
	v_pk_mul_f32 v[12:13], v[50:51], v[4:5] op_sel_hi:[1,0]
	v_add_f32_e32 v11, 1.0, v11
	v_rcp_f32_e32 v15, v5
	v_exp_f32_e64 v5, -v12
	v_rcp_f32_e32 v14, v11
	v_exp_f32_e64 v11, -v13
	v_add_f32_e32 v5, 1.0, v5
	v_pk_mul_f32 v[6:7], v[6:7], v[14:15]
	v_pk_mul_f32 v[14:15], v[42:43], v[10:11] op_sel_hi:[1,0]
	v_rcp_f32_e32 v16, v5
	v_add_f32_e32 v5, 1.0, v11
	v_pk_mul_f32 v[12:13], v[12:13], v[14:15]
	v_pk_mul_f32 v[14:15], v[44:45], v[4:5] op_sel_hi:[1,0]
	v_rcp_f32_e32 v17, v5
	v_exp_f32_e64 v5, -v14
	v_exp_f32_e64 v11, -v15
	v_pk_mul_f32 v[12:13], v[12:13], v[16:17]
	v_add_f32_e32 v5, 1.0, v5
	v_rcp_f32_e32 v18, v5
	v_add_f32_e32 v5, 1.0, v11
	v_pk_mul_f32 v[16:17], v[36:37], v[10:11] op_sel_hi:[1,0]
	v_rcp_f32_e32 v19, v5
	v_pk_mul_f32 v[4:5], v[46:47], v[4:5] op_sel_hi:[1,0]
	v_pk_mul_f32 v[14:15], v[14:15], v[16:17]
	v_exp_f32_e64 v16, -v4
	v_exp_f32_e64 v17, -v5
	v_pk_mul_f32 v[14:15], v[14:15], v[18:19]
	v_mov_b32_e32 v18, v3
	v_add_f32_e32 v16, 1.0, v16
	v_add_f32_e32 v17, 1.0, v17
	v_rcp_f32_e32 v16, v16
	v_rcp_f32_e32 v17, v17
	v_mov_b32_e32 v19, v3
	v_cvt_pk_fp8_f32 v18, v6, v7
	v_cvt_pk_fp8_f32 v19, v14, v15
	v_pk_mul_f32 v[10:11], v[38:39], v[10:11] op_sel_hi:[1,0]
	v_cvt_pk_fp8_f32 v18, v12, v13 op_sel:[0,0,1]
	v_pk_mul_f32 v[4:5], v[4:5], v[10:11]
	s_nop 0
	v_pk_mul_f32 v[4:5], v[4:5], v[16:17]
	s_nop 0
	v_cvt_pk_fp8_f32 v19, v4, v5 op_sel:[0,0,1]
	v_mov_b32_e32 v212, v18
	v_mov_b32_e32 v213, v19
	s_nop 1
	v_permlane16_swap_b32_e32 v212, v214
	v_permlane16_swap_b32_e32 v213, v215
	global_store_dwordx4 v[216:217], v[212:215], off offset:3072
	s_cbranch_vccnz .LBB0_1667
	s_andn2_b64 vcc, exec, s[48:49]
	s_cbranch_vccnz .LBB0_1666
	s_barrier
	s_branch .LBB0_1666

; __device__ __forceinline__ float rstd_fin4(const f32x4 a) { float s = (a[0] + a[1]) + (a[2] + a[3]); s += __shfl_xor(s, 16); s += __shfl_xor(s, 32); return __builtin_amdgcn_rsqf(s * (1.f / 1024.f) + 1e-6f); }
;     __device__ __forceinline__ void operator()(const f32x4 (&acc)[2][2][4][2], const Unit& u, int wr, int wc, int fr, int fq) const {
;         asm volatile("" : "+v"(fr), "+v"(fq));
;         const int row0 = u.pm * BM + wr * 64 + fr;
;         unsigned char* const hb = (unsigned char*)H + (size_t)(u.pm * (FFH / 128) + u.pn + pn0) * 32768 + (((wr * 4 + wc) * 8) * 64 + (fq >> 1) * 32 + fr * 2 + (fq & 1)) * 8;
;         f32x4 pa[2][4];
; #pragma unroll
;         for (int ai = 0; ai < 2; ++ai)
; #pragma unroll
;             for (int m = 0; m < 4; ++m) pa[ai][m] = rstd_ld4(ss, row0 + ai * HALF + m * 16, fq);
; #pragma unroll
;         for (int ai = 0; ai < 2; ++ai)
; #pragma unroll
;             for (int m = 0; m < 4; ++m) { const float rs = rstd_fin4(pa[ai][m]) * sc;
;                 const float rsl = rs * 1.4426950408889634f, rsu = rs * 0.6931471805599453f;
;                 f32x4 h0, h1;
; #pragma unroll
;                 for (int n = 0; n < 2; ++n) { const f32x4 G = acc[ai][0][m][n], U = acc[ai][1][m][n]; f32x4 hv;
; #pragma unroll
;                     for (int q = 0; q < 2; ++q) { const f32x2 g2 = (f32x2){G[2 * q], G[2 * q + 1]} * rsl, u2 = (f32x2){U[2 * q], U[2 * q + 1]} * rsu;
;                         f32x2 r2; r2.x = __builtin_amdgcn_rcpf(1.f + __builtin_amdgcn_exp2f(-g2.x)); r2.y = __builtin_amdgcn_rcpf(1.f + __builtin_amdgcn_exp2f(-g2.y));
;                         const f32x2 o2 = g2 * u2 * r2; hv[2 * q] = o2.x; hv[2 * q + 1] = o2.y; }
;                     if (n == 0) h0 = hv; else h1 = hv; }
;                 unsigned w0 = 0u, w1 = 0u;
;                 w0 = __builtin_amdgcn_cvt_pk_fp8_f32(h0[0], h0[1], w0, false); w0 = __builtin_amdgcn_cvt_pk_fp8_f32(h0[2], h0[3], w0, true); w1 = __builtin_amdgcn_cvt_pk_fp8_f32(h1[0], h1[1], w1, false); w1 = __builtin_amdgcn_cvt_pk_fp8_f32(h1[2], h1[3], w1, true);
;                 *(u32x2*)(hb + (ai * 4 + m) * 512) = (u32x2){w0, w1}; asm volatile("" ::: "memory"); }
.LBB0_1692:
	s_lshl_b32 s4, s68, 8
	v_mov_b32_e32 v14, v1
	v_mov_b32_e32 v15, v182
	s_add_i32 s4, s4, s62
	v_and_b32_e32 v17, 64, v246
	v_add_u32_e32 v4, s4, v14
	v_lshlrev_b32_e32 v6, 2, v15
	v_ashrrev_i32_e32 v7, 31, v6
	v_ashrrev_i32_e32 v5, 31, v4
	v_lshl_add_u64 v[6:7], v[6:7], 2, s[42:43]
	v_lshlrev_b64 v[4:5], 6, v[4:5]
	v_lshl_add_u64 v[12:13], v[6:7], 0, v[4:5]
	global_load_dwordx4 v[4:7], v[12:13], off
	global_load_dwordx4 v[8:11], v[12:13], off offset:1024
	global_load_dwordx4 v[28:31], v[12:13], off offset:2048
	global_load_dwordx4 v[20:23], v[12:13], off offset:3072
	v_xor_b32_e32 v16, 16, v246
	v_add_u32_e32 v17, 64, v17
	v_xor_b32_e32 v18, 32, v246
	v_cmp_lt_i32_e32 vcc, v16, v17
	v_mov_b32_e32 v32, v3
	v_mov_b32_e32 v33, v3
	v_cndmask_b32_e32 v16, v246, v16, vcc
	v_cmp_lt_i32_e32 vcc, v18, v17
	v_lshlrev_b32_e32 v27, 2, v16
	s_mul_i32 s4, s68, 22
	v_cndmask_b32_e32 v17, v246, v18, vcc
	v_lshlrev_b32_e32 v26, 2, v17
	s_add_i32 s4, s4, s67
	s_ashr_i32 s5, s4, 31
	v_lshlrev_b32_e32 v19, 4, v15
	v_lshl_add_u32 v14, v14, 1, s65
	s_lshl_b64 s[4:5], s[4:5], 15
	v_and_b32_e32 v18, 0x1fffffe0, v19
	v_and_or_b32 v14, v15, 1, v14
	v_add_lshl_u32 v14, v14, v18, 3
	s_add_u32 s4, s22, s4
	v_ashrrev_i32_e32 v15, 31, v14
	s_addc_u32 s5, s23, s5
	v_lshl_add_u64 v[24:25], s[4:5], 0, v[14:15]
	s_mov_b64 s[4:5], -1
	s_waitcnt vmcnt(0)
	v_mov_b32_e32 v16, v5
	v_mov_b32_e32 v17, v6
	v_mov_b32_e32 v5, v7
	v_mov_b32_e32 v6, v9
	v_mov_b32_e32 v7, v10
	v_mov_b32_e32 v9, v11
	v_pk_add_f32 v[4:5], v[16:17], v[4:5]
	v_pk_add_f32 v[6:7], v[6:7], v[8:9]
	v_add_f32_e32 v8, v4, v5
	v_add_f32_e32 v6, v6, v7
	ds_bpermute_b32 v7, v27, v8
	ds_bpermute_b32 v9, v27, v6
	v_add_co_u32_e32 v4, vcc, s88, v12
	s_waitcnt lgkmcnt(1)
	v_add_f32_e32 v7, v8, v7
	s_waitcnt lgkmcnt(0)
	v_add_f32_e32 v6, v6, v9
	ds_bpermute_b32 v8, v26, v7
	ds_bpermute_b32 v9, v26, v6
	v_addc_co_u32_e32 v5, vcc, 0, v13, vcc
	global_load_dwordx4 v[16:19], v[4:5], off
	global_load_dwordx4 v[12:15], v[4:5], off offset:1024
	s_waitcnt lgkmcnt(1)
	v_add_f32_e32 v7, v7, v8
	s_waitcnt lgkmcnt(0)
	v_add_f32_e32 v6, v6, v9
	v_fmamk_f32 v7, v7, 0x3a800000, v227
	v_fmamk_f32 v6, v6, 0x3a800000, v227
	v_rsq_f32_e32 v34, v7
	v_rsq_f32_e32 v35, v6
	global_load_dwordx4 v[8:11], v[4:5], off offset:2048
	s_nop 0
	global_load_dwordx4 v[4:7], v[4:5], off offset:3072
	s_andn2_b64 vcc, exec, s[40:41]
	v_mul_f32_e32 v174, 0x3c800000, v34
	v_mul_f32_e32 v35, 0x3c800000, v35
	v_mul_f32_e32 v34, 0x3fb8aa3b, v174
	v_mul_f32_e32 v174, 0x3f317218, v174
	v_pk_mul_f32 v[160:161], v[160:161], v[34:35] op_sel_hi:[1,0]
	v_pk_mul_f32 v[152:153], v[152:153], v[174:175] op_sel_hi:[1,0]
	v_pk_mul_f32 v[162:163], v[162:163], v[34:35] op_sel_hi:[1,0]
	v_pk_mul_f32 v[154:155], v[154:155], v[174:175] op_sel_hi:[1,0]
	v_pk_mul_f32 v[156:157], v[156:157], v[34:35] op_sel_hi:[1,0]
	v_mul_f32_e32 v176, 0x3fb8aa3b, v35
	v_mul_f32_e32 v178, 0x3f317218, v35
	v_pk_mul_f32 v[148:149], v[148:149], v[174:175] op_sel_hi:[1,0]
	v_pk_mul_f32 v[34:35], v[158:159], v[34:35] op_sel_hi:[1,0]
	v_exp_f32_e64 v158, -v160
	v_exp_f32_e64 v159, -v161
	v_pk_mul_f32 v[152:153], v[160:161], v[152:153]
	v_exp_f32_e64 v160, -v162
	v_exp_f32_e64 v161, -v163
	v_pk_mul_f32 v[154:155], v[162:163], v[154:155]
	v_exp_f32_e64 v162, -v156
	v_exp_f32_e64 v163, -v157
	v_pk_mul_f32 v[148:149], v[156:157], v[148:149]
	v_exp_f32_e64 v156, -v34
	v_exp_f32_e64 v157, -v35
	v_pk_mul_f32 v[150:151], v[150:151], v[174:175] op_sel_hi:[1,0]
	v_pk_mul_f32 v[144:145], v[144:145], v[176:177] op_sel_hi:[1,0]
	v_pk_mul_f32 v[34:35], v[34:35], v[150:151]
	v_add_f32_e32 v150, 1.0, v158
	v_add_f32_e32 v151, 1.0, v159
	v_add_f32_e32 v158, 1.0, v160
	v_add_f32_e32 v159, 1.0, v161
	v_add_f32_e32 v160, 1.0, v162
	v_add_f32_e32 v161, 1.0, v163
	v_add_f32_e32 v162, 1.0, v156
	v_add_f32_e32 v163, 1.0, v157
	v_rcp_f32_e32 v150, v150
	v_rcp_f32_e32 v151, v151
	v_rcp_f32_e32 v156, v158
	v_rcp_f32_e32 v157, v159
	v_rcp_f32_e32 v158, v160
	v_rcp_f32_e32 v159, v161
	v_rcp_f32_e32 v160, v162
	v_rcp_f32_e32 v161, v163
	v_pk_mul_f32 v[150:151], v[152:153], v[150:151]
	v_pk_mul_f32 v[148:149], v[148:149], v[158:159]
	v_cvt_pk_fp8_f32 v32, v150, v151
	v_cvt_pk_fp8_f32 v33, v148, v149
	v_pk_mul_f32 v[148:149], v[154:155], v[156:157]
	v_pk_mul_f32 v[34:35], v[34:35], v[160:161]
	v_cvt_pk_fp8_f32 v32, v148, v149 op_sel:[0,0,1]
	v_cvt_pk_fp8_f32 v33, v34, v35 op_sel:[0,0,1]
	v_exp_f32_e64 v35, -v145
	v_exp_f32_e64 v174, -v144
	v_pk_mul_f32 v[136:137], v[136:137], v[178:179] op_sel_hi:[1,0]
	v_and_b32_e32 v218, 16, v246
	v_mov_b32_e32 v219, 0x200
	v_cmp_eq_u32_e64 s[60:61], 0, v218
	s_nop 1
	v_cndmask_b32_e64 v218, -8, v219, s[60:61]
	v_ashrrev_i32_e32 v219, 31, v218
	v_lshl_add_u64 v[216:217], v[24:25], 0, v[218:219]
	v_mov_b32_e32 v210, v32
	v_mov_b32_e32 v211, v33
	v_add_f32_e32 v32, 1.0, v35
	v_add_f32_e32 v34, 1.0, v174
	v_rcp_f32_e32 v35, v32
	v_pk_mul_f32 v[32:33], v[144:145], v[136:137]
	v_pk_mul_f32 v[136:137], v[146:147], v[176:177] op_sel_hi:[1,0]
	v_rcp_f32_e32 v34, v34
	v_exp_f32_e64 v144, -v136
	v_exp_f32_e64 v145, -v137
	v_pk_mul_f32 v[132:133], v[132:133], v[178:179] op_sel_hi:[1,0]
	v_pk_mul_f32 v[32:33], v[32:33], v[34:35]
	v_pk_mul_f32 v[34:35], v[138:139], v[178:179] op_sel_hi:[1,0]
	v_add_f32_e32 v138, 1.0, v144
	v_add_f32_e32 v139, 1.0, v145
	v_rcp_f32_e32 v138, v138
	v_rcp_f32_e32 v139, v139
	v_pk_mul_f32 v[34:35], v[136:137], v[34:35]
	v_pk_mul_f32 v[136:137], v[140:141], v[176:177] op_sel_hi:[1,0]
	v_pk_mul_f32 v[134:135], v[134:135], v[178:179] op_sel_hi:[1,0]
	v_exp_f32_e64 v140, -v136
	v_pk_mul_f32 v[34:35], v[34:35], v[138:139]
	v_exp_f32_e64 v139, -v137
	v_pk_mul_f32 v[132:133], v[136:137], v[132:133]
	v_mov_b32_e32 v136, v29
	v_mov_b32_e32 v137, v30
	v_mov_b32_e32 v29, v31
	v_pk_add_f32 v[28:29], v[136:137], v[28:29]
	v_add_f32_e32 v138, 1.0, v140
	v_add_f32_e32 v136, v28, v29
	ds_bpermute_b32 v137, v27, v136
	v_add_f32_e32 v139, 1.0, v139
	v_rcp_f32_e32 v138, v138
	v_rcp_f32_e32 v139, v139
	v_pk_mul_f32 v[140:141], v[142:143], v[176:177] op_sel_hi:[1,0]
	s_waitcnt lgkmcnt(0)
; __device__ __forceinline__ float rstd_fin4(const f32x4 a) { float s = (a[0] + a[1]) + (a[2] + a[3]); s += __shfl_xor(s, 16); s += __shfl_xor(s, 32); return __builtin_amdgcn_rsqf(s * (1.f / 1024.f) + 1e-6f); }
;     __device__ __forceinline__ void operator()(const f32x4 (&acc)[2][2][4][2], const Unit& u, int wr, int wc, int fr, int fq) const {
;     ...
;             for (int m = 0; m < 4; ++m) { const float rs = rstd_fin4(pa[ai][m]) * sc;
;                 const float rsl = rs * 1.4426950408889634f, rsu = rs * 0.6931471805599453f;
;                 f32x4 h0, h1;
; #pragma unroll
;                 for (int n = 0; n < 2; ++n) { const f32x4 G = acc[ai][0][m][n], U = acc[ai][1][m][n]; f32x4 hv;
; #pragma unroll
;                     for (int q = 0; q < 2; ++q) { const f32x2 g2 = (f32x2){G[2 * q], G[2 * q + 1]} * rsl, u2 = (f32x2){U[2 * q], U[2 * q + 1]} * rsu;
;                         f32x2 r2; r2.x = __builtin_amdgcn_rcpf(1.f + __builtin_amdgcn_exp2f(-g2.x)); r2.y = __builtin_amdgcn_rcpf(1.f + __builtin_amdgcn_exp2f(-g2.y));
;                         const f32x2 o2 = g2 * u2 * r2; hv[2 * q] = o2.x; hv[2 * q + 1] = o2.y; }
;                     if (n == 0) h0 = hv; else h1 = hv; }
;                 unsigned w0 = 0u, w1 = 0u;
;                 w0 = __builtin_amdgcn_cvt_pk_fp8_f32(h0[0], h0[1], w0, false); w0 = __builtin_amdgcn_cvt_pk_fp8_f32(h0[2], h0[3], w0, true); w1 = __builtin_amdgcn_cvt_pk_fp8_f32(h1[0], h1[1], w1, false); w1 = __builtin_amdgcn_cvt_pk_fp8_f32(h1[2], h1[3], w1, true);
;                 *(u32x2*)(hb + (ai * 4 + m) * 512) = (u32x2){w0, w1}; asm volatile("" ::: "memory"); }
	v_add_f32_e32 v136, v136, v137
	ds_bpermute_b32 v137, v26, v136
	v_exp_f32_e64 v142, -v140
	v_pk_mul_f32 v[132:133], v[132:133], v[138:139]
	v_exp_f32_e64 v139, -v141
	v_pk_mul_f32 v[30:31], v[140:141], v[134:135]
	v_mov_b32_e32 v134, v3
	v_add_f32_e32 v138, 1.0, v142
	v_add_f32_e32 v29, 1.0, v139
	v_cvt_pk_fp8_f32 v134, v32, v33
	s_waitcnt lgkmcnt(0)
	v_add_f32_e32 v32, v136, v137
	v_rcp_f32_e32 v28, v138
	v_rcp_f32_e32 v29, v29
	v_mov_b32_e32 v135, v3
	v_fmamk_f32 v32, v32, 0x3a800000, v227
	v_cvt_pk_fp8_f32 v135, v132, v133
	v_rsq_f32_e32 v32, v32
	v_pk_mul_f32 v[28:29], v[30:31], v[28:29]
	v_cvt_pk_fp8_f32 v134, v34, v35 op_sel:[0,0,1]
	v_cvt_pk_fp8_f32 v135, v28, v29 op_sel:[0,0,1]
	v_mul_f32_e32 v29, 0x3c800000, v32
	v_mul_f32_e32 v28, 0x3fb8aa3b, v29
	v_pk_mul_f32 v[30:31], v[128:129], v[28:29] op_sel_hi:[1,0]
	v_mul_f32_e32 v32, 0x3f317218, v29
	v_exp_f32_e64 v33, -v30
	v_exp_f32_e64 v29, -v31
	v_mov_b32_e32 v208, v134
	v_mov_b32_e32 v209, v135
	s_nop 1
	v_permlane16_swap_b32_e32 v208, v210
	v_permlane16_swap_b32_e32 v209, v211
	global_store_dwordx4 v[216:217], v[208:211], off
	v_pk_mul_f32 v[34:35], v[120:121], v[32:33] op_sel_hi:[1,0]
	v_add_f32_e32 v29, 1.0, v29
	v_pk_mul_f32 v[30:31], v[30:31], v[34:35]
	v_pk_mul_f32 v[34:35], v[130:131], v[28:29] op_sel_hi:[1,0]
	v_add_f32_e32 v33, 1.0, v33
	v_rcp_f32_e32 v121, v29
	v_exp_f32_e64 v29, -v34
	v_rcp_f32_e32 v120, v33
	v_exp_f32_e64 v33, -v35
	v_add_f32_e32 v29, 1.0, v29
	v_pk_mul_f32 v[30:31], v[30:31], v[120:121]
	v_pk_mul_f32 v[120:121], v[122:123], v[32:33] op_sel_hi:[1,0]
	v_rcp_f32_e32 v122, v29
	v_add_f32_e32 v29, 1.0, v33
	v_pk_mul_f32 v[34:35], v[34:35], v[120:121]
	v_pk_mul_f32 v[120:121], v[124:125], v[28:29] op_sel_hi:[1,0]
	v_rcp_f32_e32 v123, v29
	v_exp_f32_e64 v29, -v120
	v_exp_f32_e64 v33, -v121
	v_pk_mul_f32 v[34:35], v[34:35], v[122:123]
	v_add_f32_e32 v29, 1.0, v29
	v_rcp_f32_e32 v122, v29
	v_add_f32_e32 v29, 1.0, v33
	v_pk_mul_f32 v[116:117], v[116:117], v[32:33] op_sel_hi:[1,0]
	v_rcp_f32_e32 v123, v29
	v_pk_mul_f32 v[28:29], v[126:127], v[28:29] op_sel_hi:[1,0]
	v_pk_mul_f32 v[116:117], v[120:121], v[116:117]
	v_exp_f32_e64 v120, -v28
	v_exp_f32_e64 v121, -v29
	v_pk_mul_f32 v[32:33], v[118:119], v[32:33] op_sel_hi:[1,0]
	v_pk_mul_f32 v[116:117], v[116:117], v[122:123]
	v_add_f32_e32 v118, 1.0, v120
	v_add_f32_e32 v119, 1.0, v121
	v_mov_b32_e32 v120, v21
	v_mov_b32_e32 v121, v22
	v_mov_b32_e32 v21, v23
	v_pk_add_f32 v[20:21], v[120:121], v[20:21]
	v_rcp_f32_e32 v118, v118
	v_add_f32_e32 v22, v20, v21
	ds_bpermute_b32 v23, v27, v22
	v_mov_b32_e32 v20, v3
	v_cvt_pk_fp8_f32 v20, v30, v31
	v_rcp_f32_e32 v119, v119
	v_mov_b32_e32 v21, v3
	s_waitcnt lgkmcnt(0)
	v_add_f32_e32 v30, v22, v23
	ds_bpermute_b32 v31, v26, v30
	v_cvt_pk_fp8_f32 v21, v116, v117
	v_pk_mul_f32 v[22:23], v[28:29], v[32:33]
	v_cvt_pk_fp8_f32 v20, v34, v35 op_sel:[0,0,1]
	v_pk_mul_f32 v[22:23], v[22:23], v[118:119]
	s_nop 0
	v_cvt_pk_fp8_f32 v21, v22, v23 op_sel:[0,0,1]
	s_waitcnt lgkmcnt(0)
	v_add_f32_e32 v22, v30, v31
	v_fmamk_f32 v22, v22, 0x3a800000, v227
	v_rsq_f32_e32 v22, v22
	v_mov_b32_e32 v214, v20
	v_mov_b32_e32 v215, v21
	v_mul_f32_e32 v21, 0x3c800000, v22
	v_mul_f32_e32 v20, 0x3fb8aa3b, v21
	v_pk_mul_f32 v[22:23], v[112:113], v[20:21] op_sel_hi:[1,0]
	v_mul_f32_e32 v28, 0x3f317218, v21
	v_exp_f32_e64 v29, -v22
	v_exp_f32_e64 v21, -v23
	v_pk_mul_f32 v[30:31], v[104:105], v[28:29] op_sel_hi:[1,0]
	v_add_f32_e32 v21, 1.0, v21
	v_pk_mul_f32 v[22:23], v[22:23], v[30:31]
	v_pk_mul_f32 v[30:31], v[114:115], v[20:21] op_sel_hi:[1,0]
	v_add_f32_e32 v29, 1.0, v29
	v_rcp_f32_e32 v33, v21
	v_exp_f32_e64 v21, -v30
	v_rcp_f32_e32 v32, v29
	v_exp_f32_e64 v29, -v31
	v_add_f32_e32 v21, 1.0, v21
	v_pk_mul_f32 v[22:23], v[22:23], v[32:33]
	v_pk_mul_f32 v[32:33], v[106:107], v[28:29] op_sel_hi:[1,0]
	v_rcp_f32_e32 v34, v21
	v_add_f32_e32 v21, 1.0, v29
	v_pk_mul_f32 v[30:31], v[30:31], v[32:33]
	v_pk_mul_f32 v[32:33], v[108:109], v[20:21] op_sel_hi:[1,0]
	v_rcp_f32_e32 v35, v21
	v_exp_f32_e64 v21, -v32
	v_exp_f32_e64 v29, -v33
	v_pk_mul_f32 v[30:31], v[30:31], v[34:35]
	v_add_f32_e32 v21, 1.0, v21
	v_pk_mul_f32 v[34:35], v[100:101], v[28:29] op_sel_hi:[1,0]
	v_rcp_f32_e32 v100, v21
	v_add_f32_e32 v21, 1.0, v29
	v_rcp_f32_e32 v101, v21
	v_pk_mul_f32 v[32:33], v[32:33], v[34:35]
	v_pk_mul_f32 v[20:21], v[110:111], v[20:21] op_sel_hi:[1,0]
	v_pk_mul_f32 v[28:29], v[102:103], v[28:29] op_sel_hi:[1,0]
	v_pk_mul_f32 v[32:33], v[32:33], v[100:101]
	s_waitcnt vmcnt(4)
	v_mov_b32_e32 v100, v17
	v_mov_b32_e32 v101, v18
	v_mov_b32_e32 v17, v19
	v_pk_add_f32 v[16:17], v[100:101], v[16:17]
	v_exp_f32_e64 v34, -v20
	v_add_f32_e32 v18, v16, v17
	ds_bpermute_b32 v19, v27, v18
	v_exp_f32_e64 v35, -v21
	v_mov_b32_e32 v16, v3
	v_add_f32_e32 v34, 1.0, v34
	v_cvt_pk_fp8_f32 v16, v22, v23
	v_add_f32_e32 v35, 1.0, v35
	s_waitcnt lgkmcnt(0)
	v_add_f32_e32 v22, v18, v19
	v_rcp_f32_e32 v34, v34
	v_rcp_f32_e32 v35, v35
	v_mov_b32_e32 v17, v3
	ds_bpermute_b32 v23, v26, v22
	v_cvt_pk_fp8_f32 v17, v32, v33
	v_pk_mul_f32 v[18:19], v[20:21], v[28:29]
	v_cvt_pk_fp8_f32 v16, v30, v31 op_sel:[0,0,1]
	v_pk_mul_f32 v[18:19], v[18:19], v[34:35]
	s_nop 0
	v_cvt_pk_fp8_f32 v17, v18, v19 op_sel:[0,0,1]
	s_waitcnt lgkmcnt(0)
; __device__ __forceinline__ float rstd_fin4(const f32x4 a) { float s = (a[0] + a[1]) + (a[2] + a[3]); s += __shfl_xor(s, 16); s += __shfl_xor(s, 32); return __builtin_amdgcn_rsqf(s * (1.f / 1024.f) + 1e-6f); }
;     __device__ __forceinline__ void operator()(const f32x4 (&acc)[2][2][4][2], const Unit& u, int wr, int wc, int fr, int fq) const {
;     ...
;             for (int m = 0; m < 4; ++m) { const float rs = rstd_fin4(pa[ai][m]) * sc;
;                 const float rsl = rs * 1.4426950408889634f, rsu = rs * 0.6931471805599453f;
;                 f32x4 h0, h1;
; #pragma unroll
;                 for (int n = 0; n < 2; ++n) { const f32x4 G = acc[ai][0][m][n], U = acc[ai][1][m][n]; f32x4 hv;
; #pragma unroll
;                     for (int q = 0; q < 2; ++q) { const f32x2 g2 = (f32x2){G[2 * q], G[2 * q + 1]} * rsl, u2 = (f32x2){U[2 * q], U[2 * q + 1]} * rsu;
;                         f32x2 r2; r2.x = __builtin_amdgcn_rcpf(1.f + __builtin_amdgcn_exp2f(-g2.x)); r2.y = __builtin_amdgcn_rcpf(1.f + __builtin_amdgcn_exp2f(-g2.y));
;                         const f32x2 o2 = g2 * u2 * r2; hv[2 * q] = o2.x; hv[2 * q + 1] = o2.y; }
;                     if (n == 0) h0 = hv; else h1 = hv; }
;                 unsigned w0 = 0u, w1 = 0u;
;                 w0 = __builtin_amdgcn_cvt_pk_fp8_f32(h0[0], h0[1], w0, false); w0 = __builtin_amdgcn_cvt_pk_fp8_f32(h0[2], h0[3], w0, true); w1 = __builtin_amdgcn_cvt_pk_fp8_f32(h1[0], h1[1], w1, false); w1 = __builtin_amdgcn_cvt_pk_fp8_f32(h1[2], h1[3], w1, true);
;                 *(u32x2*)(hb + (ai * 4 + m) * 512) = (u32x2){w0, w1}; asm volatile("" ::: "memory"); }
	v_add_f32_e32 v18, v22, v23
	v_fmamk_f32 v18, v18, 0x3a800000, v227
	v_rsq_f32_e32 v18, v18
	v_mov_b32_e32 v212, v16
	v_mov_b32_e32 v213, v17
	s_nop 1
	v_permlane16_swap_b32_e32 v212, v214
	v_permlane16_swap_b32_e32 v213, v215
	global_store_dwordx4 v[216:217], v[212:215], off offset:1024
	v_mul_f32_e32 v17, 0x3c800000, v18
	v_mul_f32_e32 v16, 0x3fb8aa3b, v17
	v_pk_mul_f32 v[18:19], v[96:97], v[16:17] op_sel_hi:[1,0]
	v_mul_f32_e32 v20, 0x3f317218, v17
	v_exp_f32_e64 v21, -v18
	v_exp_f32_e64 v17, -v19
	v_pk_mul_f32 v[22:23], v[88:89], v[20:21] op_sel_hi:[1,0]
	v_add_f32_e32 v17, 1.0, v17
	v_pk_mul_f32 v[18:19], v[18:19], v[22:23]
	v_pk_mul_f32 v[22:23], v[98:99], v[16:17] op_sel_hi:[1,0]
	v_add_f32_e32 v21, 1.0, v21
	v_rcp_f32_e32 v29, v17
	v_exp_f32_e64 v17, -v22
	v_rcp_f32_e32 v28, v21
	v_exp_f32_e64 v21, -v23
	v_add_f32_e32 v17, 1.0, v17
	v_pk_mul_f32 v[18:19], v[18:19], v[28:29]
	v_pk_mul_f32 v[28:29], v[90:91], v[20:21] op_sel_hi:[1,0]
	v_rcp_f32_e32 v30, v17
	v_add_f32_e32 v17, 1.0, v21
	v_pk_mul_f32 v[22:23], v[22:23], v[28:29]
	v_pk_mul_f32 v[28:29], v[92:93], v[16:17] op_sel_hi:[1,0]
	v_rcp_f32_e32 v31, v17
	v_exp_f32_e64 v21, -v29
	v_exp_f32_e64 v17, -v28
	v_pk_mul_f32 v[22:23], v[22:23], v[30:31]
	v_pk_mul_f32 v[30:31], v[84:85], v[20:21] op_sel_hi:[1,0]
	v_add_f32_e32 v17, 1.0, v17
	v_pk_mul_f32 v[28:29], v[28:29], v[30:31]
	s_waitcnt vmcnt(4)
	v_mov_b32_e32 v30, v13
	v_mov_b32_e32 v31, v14
	v_mov_b32_e32 v13, v15
	v_pk_add_f32 v[12:13], v[30:31], v[12:13]
	v_rcp_f32_e32 v32, v17
	v_add_f32_e32 v30, v12, v13
	ds_bpermute_b32 v31, v27, v30
	v_add_f32_e32 v17, 1.0, v21
	v_rcp_f32_e32 v33, v17
	v_pk_mul_f32 v[16:17], v[94:95], v[16:17] op_sel_hi:[1,0]
	v_pk_mul_f32 v[20:21], v[86:87], v[20:21] op_sel_hi:[1,0]
	v_exp_f32_e64 v34, -v16
	v_pk_mul_f32 v[14:15], v[16:17], v[20:21]
	s_waitcnt lgkmcnt(0)
	v_add_f32_e32 v20, v30, v31
	ds_bpermute_b32 v21, v26, v20
	v_pk_mul_f32 v[28:29], v[28:29], v[32:33]
	v_exp_f32_e64 v33, -v17
	v_mov_b32_e32 v16, v3
	v_add_f32_e32 v32, 1.0, v34
	v_cvt_pk_fp8_f32 v16, v18, v19
	v_add_f32_e32 v13, 1.0, v33
	s_waitcnt lgkmcnt(0)
	v_add_f32_e32 v18, v20, v21
	v_rcp_f32_e32 v12, v32
	v_rcp_f32_e32 v13, v13
	v_mov_b32_e32 v17, v3
	v_fmamk_f32 v18, v18, 0x3a800000, v227
	v_cvt_pk_fp8_f32 v17, v28, v29
	v_rsq_f32_e32 v18, v18
	v_pk_mul_f32 v[12:13], v[14:15], v[12:13]
	v_cvt_pk_fp8_f32 v16, v22, v23 op_sel:[0,0,1]
	v_cvt_pk_fp8_f32 v17, v12, v13 op_sel:[0,0,1]
	v_mul_f32_e32 v13, 0x3c800000, v18
	v_mul_f32_e32 v12, 0x3fb8aa3b, v13
	v_pk_mul_f32 v[14:15], v[80:81], v[12:13] op_sel_hi:[1,0]
	v_mul_f32_e32 v18, 0x3f317218, v13
	v_exp_f32_e64 v19, -v14
	v_exp_f32_e64 v13, -v15
	v_mov_b32_e32 v210, v16
	v_mov_b32_e32 v211, v17
	v_pk_mul_f32 v[20:21], v[72:73], v[18:19] op_sel_hi:[1,0]
	v_add_f32_e32 v13, 1.0, v13
	v_pk_mul_f32 v[14:15], v[14:15], v[20:21]
	v_pk_mul_f32 v[20:21], v[82:83], v[12:13] op_sel_hi:[1,0]
	v_add_f32_e32 v19, 1.0, v19
	v_rcp_f32_e32 v23, v13
	v_exp_f32_e64 v13, -v20
	v_rcp_f32_e32 v22, v19
	v_exp_f32_e64 v19, -v21
	v_add_f32_e32 v13, 1.0, v13
	v_pk_mul_f32 v[14:15], v[14:15], v[22:23]
	v_pk_mul_f32 v[22:23], v[74:75], v[18:19] op_sel_hi:[1,0]
	v_rcp_f32_e32 v28, v13
	v_add_f32_e32 v13, 1.0, v19
	v_pk_mul_f32 v[20:21], v[20:21], v[22:23]
	v_pk_mul_f32 v[22:23], v[76:77], v[12:13] op_sel_hi:[1,0]
	v_rcp_f32_e32 v29, v13
	v_exp_f32_e64 v13, -v22
	v_exp_f32_e64 v19, -v23
	v_pk_mul_f32 v[20:21], v[20:21], v[28:29]
	v_add_f32_e32 v13, 1.0, v13
	v_rcp_f32_e32 v30, v13
	v_add_f32_e32 v13, 1.0, v19
	v_rcp_f32_e32 v31, v13
	v_pk_mul_f32 v[28:29], v[68:69], v[18:19] op_sel_hi:[1,0]
	v_pk_mul_f32 v[12:13], v[78:79], v[12:13] op_sel_hi:[1,0]
	v_pk_mul_f32 v[22:23], v[22:23], v[28:29]
	v_exp_f32_e64 v28, -v12
	v_pk_mul_f32 v[22:23], v[22:23], v[30:31]
	s_waitcnt vmcnt(3)
	v_mov_b32_e32 v30, v9
	v_mov_b32_e32 v31, v10
	v_mov_b32_e32 v9, v11
	v_pk_add_f32 v[8:9], v[30:31], v[8:9]
	v_exp_f32_e64 v29, -v13
	v_add_f32_e32 v10, v8, v9
	ds_bpermute_b32 v11, v27, v10
	v_mov_b32_e32 v8, v3
	v_add_f32_e32 v28, 1.0, v28
	v_add_f32_e32 v29, 1.0, v29
	v_cvt_pk_fp8_f32 v8, v14, v15
	s_waitcnt lgkmcnt(0)
	v_add_f32_e32 v14, v10, v11
	v_rcp_f32_e32 v28, v28
	v_rcp_f32_e32 v29, v29
	v_mov_b32_e32 v9, v3
	ds_bpermute_b32 v15, v26, v14
	v_cvt_pk_fp8_f32 v9, v22, v23
	v_pk_mul_f32 v[18:19], v[70:71], v[18:19] op_sel_hi:[1,0]
	v_cvt_pk_fp8_f32 v8, v20, v21 op_sel:[0,0,1]
	v_pk_mul_f32 v[10:11], v[12:13], v[18:19]
	s_nop 0
	v_pk_mul_f32 v[10:11], v[10:11], v[28:29]
	s_nop 0
	v_cvt_pk_fp8_f32 v9, v10, v11 op_sel:[0,0,1]
	s_waitcnt lgkmcnt(0)
; __device__ __forceinline__ float rstd_fin4(const f32x4 a) { float s = (a[0] + a[1]) + (a[2] + a[3]); s += __shfl_xor(s, 16); s += __shfl_xor(s, 32); return __builtin_amdgcn_rsqf(s * (1.f / 1024.f) + 1e-6f); }
;     __device__ __forceinline__ void operator()(const f32x4 (&acc)[2][2][4][2], const Unit& u, int wr, int wc, int fr, int fq) const {
;     ...
;             for (int m = 0; m < 4; ++m) { const float rs = rstd_fin4(pa[ai][m]) * sc;
;                 const float rsl = rs * 1.4426950408889634f, rsu = rs * 0.6931471805599453f;
;                 f32x4 h0, h1;
; #pragma unroll
;                 for (int n = 0; n < 2; ++n) { const f32x4 G = acc[ai][0][m][n], U = acc[ai][1][m][n]; f32x4 hv;
; #pragma unroll
;                     for (int q = 0; q < 2; ++q) { const f32x2 g2 = (f32x2){G[2 * q], G[2 * q + 1]} * rsl, u2 = (f32x2){U[2 * q], U[2 * q + 1]} * rsu;
;                         f32x2 r2; r2.x = __builtin_amdgcn_rcpf(1.f + __builtin_amdgcn_exp2f(-g2.x)); r2.y = __builtin_amdgcn_rcpf(1.f + __builtin_amdgcn_exp2f(-g2.y));
;                         const f32x2 o2 = g2 * u2 * r2; hv[2 * q] = o2.x; hv[2 * q + 1] = o2.y; }
;                     if (n == 0) h0 = hv; else h1 = hv; }
;                 unsigned w0 = 0u, w1 = 0u;
;                 w0 = __builtin_amdgcn_cvt_pk_fp8_f32(h0[0], h0[1], w0, false); w0 = __builtin_amdgcn_cvt_pk_fp8_f32(h0[2], h0[3], w0, true); w1 = __builtin_amdgcn_cvt_pk_fp8_f32(h1[0], h1[1], w1, false); w1 = __builtin_amdgcn_cvt_pk_fp8_f32(h1[2], h1[3], w1, true);
;                 *(u32x2*)(hb + (ai * 4 + m) * 512) = (u32x2){w0, w1}; asm volatile("" ::: "memory"); }
	v_add_f32_e32 v10, v14, v15
	v_fmamk_f32 v10, v10, 0x3a800000, v227
	v_rsq_f32_e32 v10, v10
	v_mov_b32_e32 v208, v8
	v_mov_b32_e32 v209, v9
	s_nop 1
	v_permlane16_swap_b32_e32 v208, v210
	v_permlane16_swap_b32_e32 v209, v211
	global_store_dwordx4 v[216:217], v[208:211], off offset:2048
	v_mul_f32_e32 v9, 0x3c800000, v10
	v_mul_f32_e32 v8, 0x3fb8aa3b, v9
	v_pk_mul_f32 v[10:11], v[64:65], v[8:9] op_sel_hi:[1,0]
	v_mul_f32_e32 v12, 0x3f317218, v9
	v_exp_f32_e64 v13, -v10
	v_exp_f32_e64 v9, -v11
	v_pk_mul_f32 v[14:15], v[56:57], v[12:13] op_sel_hi:[1,0]
	v_add_f32_e32 v9, 1.0, v9
	v_pk_mul_f32 v[10:11], v[10:11], v[14:15]
	v_pk_mul_f32 v[14:15], v[66:67], v[8:9] op_sel_hi:[1,0]
	v_add_f32_e32 v13, 1.0, v13
	v_rcp_f32_e32 v17, v9
	v_exp_f32_e64 v9, -v14
	v_rcp_f32_e32 v16, v13
	v_exp_f32_e64 v13, -v15
	v_add_f32_e32 v9, 1.0, v9
	v_pk_mul_f32 v[10:11], v[10:11], v[16:17]
	v_pk_mul_f32 v[16:17], v[58:59], v[12:13] op_sel_hi:[1,0]
	v_rcp_f32_e32 v18, v9
	v_add_f32_e32 v9, 1.0, v13
	v_pk_mul_f32 v[14:15], v[14:15], v[16:17]
	v_pk_mul_f32 v[16:17], v[60:61], v[8:9] op_sel_hi:[1,0]
	v_rcp_f32_e32 v19, v9
	v_exp_f32_e64 v13, -v17
	v_exp_f32_e64 v9, -v16
	v_pk_mul_f32 v[14:15], v[14:15], v[18:19]
	v_pk_mul_f32 v[18:19], v[52:53], v[12:13] op_sel_hi:[1,0]
	v_add_f32_e32 v9, 1.0, v9
	v_pk_mul_f32 v[16:17], v[16:17], v[18:19]
	s_waitcnt vmcnt(3)
	v_mov_b32_e32 v18, v5
	v_mov_b32_e32 v19, v6
	v_mov_b32_e32 v5, v7
	v_pk_add_f32 v[4:5], v[18:19], v[4:5]
	v_rcp_f32_e32 v20, v9
	v_add_f32_e32 v18, v4, v5
	ds_bpermute_b32 v19, v27, v18
	v_add_f32_e32 v9, 1.0, v13
	v_rcp_f32_e32 v21, v9
	v_pk_mul_f32 v[8:9], v[62:63], v[8:9] op_sel_hi:[1,0]
	v_pk_mul_f32 v[12:13], v[54:55], v[12:13] op_sel_hi:[1,0]
	v_exp_f32_e64 v22, -v8
	v_pk_mul_f32 v[6:7], v[8:9], v[12:13]
	s_waitcnt lgkmcnt(0)
	v_add_f32_e32 v12, v18, v19
	ds_bpermute_b32 v13, v26, v12
	v_pk_mul_f32 v[16:17], v[16:17], v[20:21]
	v_exp_f32_e64 v21, -v9
	v_mov_b32_e32 v8, v3
	v_add_f32_e32 v20, 1.0, v22
	v_cvt_pk_fp8_f32 v8, v10, v11
	v_add_f32_e32 v5, 1.0, v21
	s_waitcnt lgkmcnt(0)
	v_add_f32_e32 v10, v12, v13
	v_rcp_f32_e32 v4, v20
	v_rcp_f32_e32 v5, v5
	v_mov_b32_e32 v9, v3
	v_fmamk_f32 v10, v10, 0x3a800000, v227
	v_cvt_pk_fp8_f32 v9, v16, v17
	v_rsq_f32_e32 v10, v10
	v_pk_mul_f32 v[4:5], v[6:7], v[4:5]
	v_cvt_pk_fp8_f32 v8, v14, v15 op_sel:[0,0,1]
	v_cvt_pk_fp8_f32 v9, v4, v5 op_sel:[0,0,1]
	v_mul_f32_e32 v5, 0x3c800000, v10
	v_mul_f32_e32 v4, 0x3fb8aa3b, v5
	v_pk_mul_f32 v[6:7], v[48:49], v[4:5] op_sel_hi:[1,0]
	v_mul_f32_e32 v10, 0x3f317218, v5
	v_exp_f32_e64 v11, -v6
	v_exp_f32_e64 v5, -v7
	v_mov_b32_e32 v214, v8
	v_mov_b32_e32 v215, v9
	v_pk_mul_f32 v[12:13], v[40:41], v[10:11] op_sel_hi:[1,0]
	v_add_f32_e32 v5, 1.0, v5
	v_pk_mul_f32 v[6:7], v[6:7], v[12:13]
	v_pk_mul_f32 v[12:13], v[50:51], v[4:5] op_sel_hi:[1,0]
	v_add_f32_e32 v11, 1.0, v11
	v_rcp_f32_e32 v15, v5
	v_exp_f32_e64 v5, -v12
	v_rcp_f32_e32 v14, v11
	v_exp_f32_e64 v11, -v13
	v_add_f32_e32 v5, 1.0, v5
	v_pk_mul_f32 v[6:7], v[6:7], v[14:15]
	v_pk_mul_f32 v[14:15], v[42:43], v[10:11] op_sel_hi:[1,0]
	v_rcp_f32_e32 v16, v5
	v_add_f32_e32 v5, 1.0, v11
	v_pk_mul_f32 v[12:13], v[12:13], v[14:15]
	v_pk_mul_f32 v[14:15], v[44:45], v[4:5] op_sel_hi:[1,0]
	v_rcp_f32_e32 v17, v5
	v_exp_f32_e64 v5, -v14
	v_exp_f32_e64 v11, -v15
	v_pk_mul_f32 v[12:13], v[12:13], v[16:17]
	v_add_f32_e32 v5, 1.0, v5
	v_rcp_f32_e32 v18, v5
	v_add_f32_e32 v5, 1.0, v11
	v_pk_mul_f32 v[16:17], v[36:37], v[10:11] op_sel_hi:[1,0]
	v_rcp_f32_e32 v19, v5
	v_pk_mul_f32 v[4:5], v[46:47], v[4:5] op_sel_hi:[1,0]
	v_pk_mul_f32 v[14:15], v[14:15], v[16:17]
	v_exp_f32_e64 v16, -v4
	v_exp_f32_e64 v17, -v5
	v_pk_mul_f32 v[14:15], v[14:15], v[18:19]
	v_mov_b32_e32 v18, v3
	v_add_f32_e32 v16, 1.0, v16
	v_add_f32_e32 v17, 1.0, v17
	v_rcp_f32_e32 v16, v16
	v_rcp_f32_e32 v17, v17
	v_mov_b32_e32 v19, v3
	v_cvt_pk_fp8_f32 v18, v6, v7
	v_cvt_pk_fp8_f32 v19, v14, v15
	v_pk_mul_f32 v[10:11], v[38:39], v[10:11] op_sel_hi:[1,0]
	v_cvt_pk_fp8_f32 v18, v12, v13 op_sel:[0,0,1]
	v_pk_mul_f32 v[4:5], v[4:5], v[10:11]
	s_nop 0
	v_pk_mul_f32 v[4:5], v[4:5], v[16:17]
	s_nop 0
	v_cvt_pk_fp8_f32 v19, v4, v5 op_sel:[0,0,1]
	v_mov_b32_e32 v212, v18
	v_mov_b32_e32 v213, v19
	s_nop 1
	v_permlane16_swap_b32_e32 v212, v214
	v_permlane16_swap_b32_e32 v213, v215
	global_store_dwordx4 v[216:217], v[212:215], off offset:3072
	s_cbranch_vccnz .LBB0_1685
	s_andn2_b64 vcc, exec, s[38:39]
	s_cbranch_vccnz .LBB0_1684
	s_barrier
	s_branch .LBB0_1684

; __device__ __forceinline__ float rstd_fin4(const f32x4 a) { float s = (a[0] + a[1]) + (a[2] + a[3]); s += __shfl_xor(s, 16); s += __shfl_xor(s, 32); return __builtin_amdgcn_rsqf(s * (1.f / 1024.f) + 1e-6f); }
;     __device__ __forceinline__ void operator()(const f32x4 (&acc)[2][2][4][2], const Unit& u, int wr, int wc, int fr, int fq) const {
;     ...
;         const int row0 = u.pm * BM + wr * 64 + fr;
;         unsigned char* const hb = (unsigned char*)H + (size_t)(u.pm * (FFH / 128) + u.pn + pn0) * 32768 + (((wr * 4 + wc) * 8) * 64 + (fq >> 1) * 32 + fr * 2 + (fq & 1)) * 8;
;         f32x4 pa[2][4];
; #pragma unroll
;         for (int ai = 0; ai < 2; ++ai)
; #pragma unroll
;             for (int m = 0; m < 4; ++m) pa[ai][m] = rstd_ld4(ss, row0 + ai * HALF + m * 16, fq);
; #pragma unroll
;         for (int ai = 0; ai < 2; ++ai)
; #pragma unroll
;             for (int m = 0; m < 4; ++m) { const float rs = rstd_fin4(pa[ai][m]) * sc;
;                 const float rsl = rs * 1.4426950408889634f, rsu = rs * 0.6931471805599453f;
;                 f32x4 h0, h1;
; #pragma unroll
;                 for (int n = 0; n < 2; ++n) { const f32x4 G = acc[ai][0][m][n], U = acc[ai][1][m][n]; f32x4 hv;
; #pragma unroll
;                     for (int q = 0; q < 2; ++q) { const f32x2 g2 = (f32x2){G[2 * q], G[2 * q + 1]} * rsl, u2 = (f32x2){U[2 * q], U[2 * q + 1]} * rsu;
;                         f32x2 r2; r2.x = __builtin_amdgcn_rcpf(1.f + __builtin_amdgcn_exp2f(-g2.x)); r2.y = __builtin_amdgcn_rcpf(1.f + __builtin_amdgcn_exp2f(-g2.y));
.LBB0_1712:
	s_lshl_b32 s4, s70, 8
	v_mov_b32_e32 v142, v168
	v_mov_b32_e32 v143, v1
	s_add_i32 s4, s4, s64
	v_and_b32_e32 v145, 64, v246
	v_add_u32_e32 v124, s4, v143
	v_lshlrev_b32_e32 v126, 2, v142
	v_ashrrev_i32_e32 v127, 31, v126
	v_ashrrev_i32_e32 v125, 31, v124
	v_lshl_add_u64 v[126:127], v[126:127], 2, s[44:45]
	v_lshlrev_b64 v[124:125], 6, v[124:125]
	v_lshl_add_u64 v[140:141], v[126:127], 0, v[124:125]
	global_load_dwordx4 v[136:139], v[140:141], off
	global_load_dwordx4 v[124:127], v[140:141], off offset:1024
	global_load_dwordx4 v[152:155], v[140:141], off offset:2048
	global_load_dwordx4 v[148:151], v[140:141], off offset:3072
	v_xor_b32_e32 v144, 16, v246
	v_add_u32_e32 v145, 64, v145
	v_xor_b32_e32 v146, 32, v246
	v_cmp_lt_i32_e32 vcc, v144, v145
	v_mov_b32_e32 v174, v3
	v_mov_b32_e32 v175, v3
	v_cndmask_b32_e32 v144, v246, v144, vcc
	v_cmp_lt_i32_e32 vcc, v146, v145
	v_lshlrev_b32_e32 v172, 2, v144
	s_mul_i32 s4, s70, 22
	v_cndmask_b32_e32 v145, v246, v146, vcc
	v_lshlrev_b32_e32 v171, 2, v145
	s_add_i32 s4, s69, s4
	s_add_i32 s4, s4, 18
	v_lshlrev_b32_e32 v147, 4, v142
	v_lshl_add_u32 v143, v143, 1, s67
	s_ashr_i32 s5, s4, 31
	v_and_b32_e32 v146, 0x1fffffe0, v147
	v_and_or_b32 v142, v142, 1, v143
	s_lshl_b64 s[4:5], s[4:5], 15
	v_add_lshl_u32 v142, v142, v146, 3
	s_add_u32 s4, s6, s4
	v_ashrrev_i32_e32 v143, 31, v142
	s_addc_u32 s5, s7, s5
	v_lshl_add_u64 v[166:167], s[4:5], 0, v[142:143]
	s_mov_b64 s[4:5], -1
	s_waitcnt vmcnt(0)
	v_mov_b32_e32 v144, v137
	v_mov_b32_e32 v145, v138
	v_mov_b32_e32 v137, v139
	v_mov_b32_e32 v138, v125
	v_mov_b32_e32 v139, v126
	v_mov_b32_e32 v125, v127
	v_pk_add_f32 v[126:127], v[144:145], v[136:137]
	v_pk_add_f32 v[124:125], v[138:139], v[124:125]
	v_add_f32_e32 v126, v126, v127
	v_add_f32_e32 v127, v124, v125
	ds_bpermute_b32 v136, v172, v126
	ds_bpermute_b32 v137, v172, v127
	v_add_co_u32_e32 v124, vcc, s88, v140
	s_waitcnt lgkmcnt(1)
	v_add_f32_e32 v126, v126, v136
	s_waitcnt lgkmcnt(0)
	v_add_f32_e32 v127, v127, v137
	ds_bpermute_b32 v136, v171, v126
	ds_bpermute_b32 v137, v171, v127
	v_addc_co_u32_e32 v125, vcc, 0, v141, vcc
	global_load_dwordx4 v[144:147], v[124:125], off
	global_load_dwordx4 v[140:143], v[124:125], off offset:1024
	s_waitcnt lgkmcnt(1)
	v_add_f32_e32 v126, v126, v136
	s_waitcnt lgkmcnt(0)
	v_add_f32_e32 v127, v127, v137
	v_fmamk_f32 v126, v126, 0x3a800000, v227
	v_fmamk_f32 v127, v127, 0x3a800000, v227
	v_rsq_f32_e32 v173, v126
	v_rsq_f32_e32 v177, v127
	global_load_dwordx4 v[136:139], v[124:125], off offset:2048
	s_nop 0
	global_load_dwordx4 v[124:127], v[124:125], off offset:3072
	s_andn2_b64 vcc, exec, s[40:41]
	v_mul_f32_e32 v176, 0x3fb8aa3b, v173
	v_mul_f32_e32 v178, 0x3f317218, v173
	v_pk_mul_f32 v[132:133], v[132:133], v[176:177] op_sel_hi:[1,0]
	v_pk_mul_f32 v[120:121], v[120:121], v[178:179] op_sel_hi:[1,0]
	v_pk_mul_f32 v[134:135], v[134:135], v[176:177] op_sel_hi:[1,0]
	v_pk_mul_f32 v[122:123], v[122:123], v[178:179] op_sel_hi:[1,0]
	v_pk_mul_f32 v[128:129], v[128:129], v[176:177] op_sel_hi:[1,0]
	v_pk_mul_f32 v[116:117], v[116:117], v[178:179] op_sel_hi:[1,0]
	v_pk_mul_f32 v[130:131], v[130:131], v[176:177] op_sel_hi:[1,0]
	v_exp_f32_e64 v173, -v132
	v_exp_f32_e64 v176, -v133
	v_pk_mul_f32 v[120:121], v[132:133], v[120:121]
	v_exp_f32_e64 v132, -v134
	v_exp_f32_e64 v133, -v135
	v_pk_mul_f32 v[122:123], v[134:135], v[122:123]
	v_exp_f32_e64 v134, -v128
	v_exp_f32_e64 v135, -v129
	v_pk_mul_f32 v[116:117], v[128:129], v[116:117]
	v_exp_f32_e64 v128, -v130
	v_exp_f32_e64 v129, -v131
	v_pk_mul_f32 v[118:119], v[118:119], v[178:179] op_sel_hi:[1,0]
	v_add_f32_e32 v132, 1.0, v132
	v_pk_mul_f32 v[118:119], v[130:131], v[118:119]
	v_add_f32_e32 v130, 1.0, v173
	v_add_f32_e32 v131, 1.0, v176
	v_add_f32_e32 v173, 1.0, v128
	v_add_f32_e32 v176, 1.0, v129
	v_rcp_f32_e32 v128, v130
	v_rcp_f32_e32 v129, v131
	v_add_f32_e32 v133, 1.0, v133
	v_add_f32_e32 v134, 1.0, v134
	v_add_f32_e32 v135, 1.0, v135
	v_rcp_f32_e32 v130, v132
	v_rcp_f32_e32 v131, v133
	v_rcp_f32_e32 v132, v134
	v_rcp_f32_e32 v133, v135
	v_pk_mul_f32 v[120:121], v[120:121], v[128:129]
	v_mul_f32_e32 v180, 0x3fb8aa3b, v177
	v_cvt_pk_fp8_f32 v174, v120, v121
	v_mul_f32_e32 v182, 0x3f317218, v177
	v_pk_mul_f32 v[116:117], v[116:117], v[132:133]
	v_pk_mul_f32 v[112:113], v[112:113], v[180:181] op_sel_hi:[1,0]
	v_pk_mul_f32 v[108:109], v[108:109], v[182:183] op_sel_hi:[1,0]
	v_cvt_pk_fp8_f32 v175, v116, v117
	v_pk_mul_f32 v[116:117], v[122:123], v[130:131]
	v_exp_f32_e64 v177, -v112
	v_cvt_pk_fp8_f32 v174, v116, v117 op_sel:[0,0,1]
	v_exp_f32_e64 v117, -v113
	v_pk_mul_f32 v[108:109], v[112:113], v[108:109]
	v_pk_mul_f32 v[112:113], v[114:115], v[180:181] op_sel_hi:[1,0]
	v_pk_mul_f32 v[110:111], v[110:111], v[182:183] op_sel_hi:[1,0]
	v_exp_f32_e64 v114, -v112
	v_exp_f32_e64 v115, -v113
	v_pk_mul_f32 v[104:105], v[104:105], v[180:181] op_sel_hi:[1,0]
	v_pk_mul_f32 v[110:111], v[112:113], v[110:111]
	v_add_f32_e32 v114, 1.0, v114
	v_add_f32_e32 v115, 1.0, v115
	v_exp_f32_e64 v112, -v104
	v_exp_f32_e64 v113, -v105
	v_rcp_f32_e32 v114, v114
	v_rcp_f32_e32 v115, v115
	v_add_f32_e32 v112, 1.0, v112
	v_add_f32_e32 v113, 1.0, v113
	v_pk_mul_f32 v[106:107], v[106:107], v[180:181] op_sel_hi:[1,0]
	v_pk_mul_f32 v[110:111], v[110:111], v[114:115]
	v_rcp_f32_e32 v112, v112
	v_rcp_f32_e32 v113, v113
	v_exp_f32_e64 v114, -v106
	v_pk_mul_f32 v[100:101], v[100:101], v[182:183] op_sel_hi:[1,0]
	v_add_f32_e32 v116, 1.0, v177
	v_pk_mul_f32 v[100:101], v[104:105], v[100:101]
	v_mov_b32_e32 v104, v153
	v_mov_b32_e32 v105, v154
	v_mov_b32_e32 v153, v155
	v_pk_add_f32 v[104:105], v[104:105], v[152:153]
	v_pk_mul_f32 v[100:101], v[100:101], v[112:113]
	v_add_f32_e32 v112, 1.0, v114
	v_add_f32_e32 v114, v104, v105
	ds_bpermute_b32 v115, v172, v114
	v_exp_f32_e64 v113, -v107
	v_rcp_f32_e32 v104, v112
	v_add_f32_e32 v117, 1.0, v117
	v_rcp_f32_e32 v116, v116
	s_waitcnt lgkmcnt(0)
; __device__ __forceinline__ float rstd_fin4(const f32x4 a) { float s = (a[0] + a[1]) + (a[2] + a[3]); s += __shfl_xor(s, 16); s += __shfl_xor(s, 32); return __builtin_amdgcn_rsqf(s * (1.f / 1024.f) + 1e-6f); }
;     __device__ __forceinline__ void operator()(const f32x4 (&acc)[2][2][4][2], const Unit& u, int wr, int wc, int fr, int fq) const {
;     ...
;             for (int m = 0; m < 4; ++m) { const float rs = rstd_fin4(pa[ai][m]) * sc;
;                 const float rsl = rs * 1.4426950408889634f, rsu = rs * 0.6931471805599453f;
;                 f32x4 h0, h1;
; #pragma unroll
;                 for (int n = 0; n < 2; ++n) { const f32x4 G = acc[ai][0][m][n], U = acc[ai][1][m][n]; f32x4 hv;
; #pragma unroll
;                     for (int q = 0; q < 2; ++q) { const f32x2 g2 = (f32x2){G[2 * q], G[2 * q + 1]} * rsl, u2 = (f32x2){U[2 * q], U[2 * q + 1]} * rsu;
;                         f32x2 r2; r2.x = __builtin_amdgcn_rcpf(1.f + __builtin_amdgcn_exp2f(-g2.x)); r2.y = __builtin_amdgcn_rcpf(1.f + __builtin_amdgcn_exp2f(-g2.y));
;                         const f32x2 o2 = g2 * u2 * r2; hv[2 * q] = o2.x; hv[2 * q + 1] = o2.y; }
;                     if (n == 0) h0 = hv; else h1 = hv; }
;                 unsigned w0 = 0u, w1 = 0u;
;                 w0 = __builtin_amdgcn_cvt_pk_fp8_f32(h0[0], h0[1], w0, false); w0 = __builtin_amdgcn_cvt_pk_fp8_f32(h0[2], h0[3], w0, true); w1 = __builtin_amdgcn_cvt_pk_fp8_f32(h1[0], h1[1], w1, false); w1 = __builtin_amdgcn_cvt_pk_fp8_f32(h1[2], h1[3], w1, true);
;                 *(u32x2*)(hb + (ai * 4 + m) * 512) = (u32x2){w0, w1}; asm volatile("" ::: "memory"); }
	v_add_f32_e32 v112, v114, v115
	v_add_f32_e32 v105, 1.0, v113
	ds_bpermute_b32 v113, v171, v112
	v_rcp_f32_e32 v117, v117
	v_pk_mul_f32 v[102:103], v[102:103], v[182:183] op_sel_hi:[1,0]
	v_rcp_f32_e32 v105, v105
	v_pk_mul_f32 v[102:103], v[106:107], v[102:103]
	v_mov_b32_e32 v107, v3
	v_cvt_pk_fp8_f32 v107, v100, v101
	s_waitcnt lgkmcnt(0)
	v_add_f32_e32 v100, v112, v113
	v_pk_mul_f32 v[108:109], v[108:109], v[116:117]
	v_mov_b32_e32 v106, v3
	v_fmamk_f32 v100, v100, 0x3a800000, v227
	v_cvt_pk_fp8_f32 v106, v108, v109
	v_rsq_f32_e32 v108, v100
	v_pk_mul_f32 v[100:101], v[102:103], v[104:105]
	v_rcp_f32_e32 v134, v173
	v_cvt_pk_fp8_f32 v107, v100, v101 op_sel:[0,0,1]
	v_mul_f32_e32 v100, 0x3fb8aa3b, v108
	v_pk_mul_f32 v[96:97], v[96:97], v[100:101] op_sel_hi:[1,0]
	v_mul_f32_e32 v102, 0x3f317218, v108
	v_exp_f32_e64 v101, -v96
	v_exp_f32_e64 v103, -v97
	v_rcp_f32_e32 v135, v176
	v_cvt_pk_fp8_f32 v106, v110, v111 op_sel:[0,0,1]
	v_add_f32_e32 v101, 1.0, v101
	v_pk_mul_f32 v[92:93], v[92:93], v[102:103] op_sel_hi:[1,0]
	v_rcp_f32_e32 v104, v101
	v_add_f32_e32 v101, 1.0, v103
	v_pk_mul_f32 v[92:93], v[96:97], v[92:93]
	v_pk_mul_f32 v[96:97], v[98:99], v[100:101] op_sel_hi:[1,0]
	v_pk_mul_f32 v[94:95], v[94:95], v[102:103] op_sel_hi:[1,0]
	v_pk_mul_f32 v[88:89], v[88:89], v[100:101] op_sel_hi:[1,0]
	v_exp_f32_e64 v98, -v96
	v_exp_f32_e64 v99, -v97
	v_pk_mul_f32 v[94:95], v[96:97], v[94:95]
	v_exp_f32_e64 v96, -v88
	v_exp_f32_e64 v97, -v89
	v_add_f32_e32 v98, 1.0, v98
	v_add_f32_e32 v99, 1.0, v99
	v_add_f32_e32 v96, 1.0, v96
	v_add_f32_e32 v97, 1.0, v97
	v_rcp_f32_e32 v96, v96
	v_rcp_f32_e32 v97, v97
	v_rcp_f32_e32 v98, v98
	v_rcp_f32_e32 v99, v99
	v_pk_mul_f32 v[84:85], v[84:85], v[102:103] op_sel_hi:[1,0]
	v_rcp_f32_e32 v105, v101
	v_pk_mul_f32 v[84:85], v[88:89], v[84:85]
	v_pk_mul_f32 v[94:95], v[94:95], v[98:99]
	v_pk_mul_f32 v[84:85], v[84:85], v[96:97]
	v_mov_b32_e32 v96, v149
	v_mov_b32_e32 v97, v150
	v_mov_b32_e32 v149, v151
	v_pk_add_f32 v[96:97], v[96:97], v[148:149]
	v_pk_mul_f32 v[88:89], v[90:91], v[100:101] op_sel_hi:[1,0]
	v_add_f32_e32 v98, v96, v97
	ds_bpermute_b32 v99, v172, v98
	v_exp_f32_e64 v90, -v88
	v_exp_f32_e64 v91, -v89
	v_pk_mul_f32 v[92:93], v[92:93], v[104:105]
	v_mov_b32_e32 v96, v3
	v_add_f32_e32 v90, 1.0, v90
	v_add_f32_e32 v91, 1.0, v91
	v_cvt_pk_fp8_f32 v96, v92, v93
	s_waitcnt lgkmcnt(0)
	v_add_f32_e32 v92, v98, v99
	v_rcp_f32_e32 v90, v90
	v_rcp_f32_e32 v91, v91
	v_mov_b32_e32 v97, v3
	ds_bpermute_b32 v93, v171, v92
	v_cvt_pk_fp8_f32 v97, v84, v85
	v_pk_mul_f32 v[86:87], v[86:87], v[102:103] op_sel_hi:[1,0]
	v_pk_mul_f32 v[118:119], v[118:119], v[134:135]
	v_pk_mul_f32 v[84:85], v[88:89], v[86:87]
	v_cvt_pk_fp8_f32 v175, v118, v119 op_sel:[0,0,1]
	v_pk_mul_f32 v[84:85], v[84:85], v[90:91]
	v_cvt_pk_fp8_f32 v96, v94, v95 op_sel:[0,0,1]
	v_cvt_pk_fp8_f32 v97, v84, v85 op_sel:[0,0,1]
	s_waitcnt lgkmcnt(0)
	v_add_f32_e32 v84, v92, v93
	v_fmamk_f32 v84, v84, 0x3a800000, v227
	v_rsq_f32_e32 v85, v84
	v_and_b32_e32 v218, 16, v246
	v_mov_b32_e32 v219, 0x200
	v_cmp_eq_u32_e64 s[60:61], 0, v218
	s_nop 1
	v_cndmask_b32_e64 v218, -8, v219, s[60:61]
	v_ashrrev_i32_e32 v219, 31, v218
	v_lshl_add_u64 v[216:217], v[166:167], 0, v[218:219]
	v_mov_b32_e32 v210, v174
	v_mov_b32_e32 v211, v175
	v_mov_b32_e32 v208, v106
	v_mov_b32_e32 v209, v107
	s_nop 1
	v_permlane16_swap_b32_e32 v208, v210
	v_permlane16_swap_b32_e32 v209, v211
	global_store_dwordx4 v[216:217], v[208:211], off
	v_mul_f32_e32 v84, 0x3fb8aa3b, v85
	v_pk_mul_f32 v[80:81], v[80:81], v[84:85] op_sel_hi:[1,0]
	v_mul_f32_e32 v86, 0x3f317218, v85
	v_exp_f32_e64 v87, -v80
	v_exp_f32_e64 v85, -v81
	v_mov_b32_e32 v214, v96
	v_mov_b32_e32 v215, v97
	v_pk_mul_f32 v[76:77], v[76:77], v[86:87] op_sel_hi:[1,0]
	v_add_f32_e32 v87, 1.0, v87
	v_add_f32_e32 v85, 1.0, v85
	v_pk_mul_f32 v[76:77], v[80:81], v[76:77]
	v_pk_mul_f32 v[80:81], v[82:83], v[84:85] op_sel_hi:[1,0]
	v_pk_mul_f32 v[78:79], v[78:79], v[86:87] op_sel_hi:[1,0]
	v_pk_mul_f32 v[72:73], v[72:73], v[84:85] op_sel_hi:[1,0]
	v_exp_f32_e64 v82, -v80
	v_exp_f32_e64 v83, -v81
	v_pk_mul_f32 v[78:79], v[80:81], v[78:79]
	v_exp_f32_e64 v80, -v72
	v_exp_f32_e64 v81, -v73
	v_add_f32_e32 v82, 1.0, v82
	v_add_f32_e32 v83, 1.0, v83
	v_add_f32_e32 v80, 1.0, v80
	v_add_f32_e32 v81, 1.0, v81
	v_rcp_f32_e32 v80, v80
	v_rcp_f32_e32 v81, v81
	v_rcp_f32_e32 v82, v82
	v_rcp_f32_e32 v83, v83
	v_pk_mul_f32 v[68:69], v[68:69], v[86:87] op_sel_hi:[1,0]
	v_rcp_f32_e32 v88, v87
	v_pk_mul_f32 v[68:69], v[72:73], v[68:69]
	v_pk_mul_f32 v[78:79], v[78:79], v[82:83]
	v_pk_mul_f32 v[68:69], v[68:69], v[80:81]
	s_waitcnt vmcnt(4)
	v_mov_b32_e32 v80, v145
	v_mov_b32_e32 v81, v146
	v_mov_b32_e32 v145, v147
	v_pk_add_f32 v[80:81], v[80:81], v[144:145]
	v_rcp_f32_e32 v89, v85
	v_add_f32_e32 v82, v80, v81
	v_pk_mul_f32 v[72:73], v[74:75], v[84:85] op_sel_hi:[1,0]
	ds_bpermute_b32 v83, v172, v82
	v_exp_f32_e64 v74, -v72
	v_exp_f32_e64 v75, -v73
	v_pk_mul_f32 v[76:77], v[76:77], v[88:89]
	v_mov_b32_e32 v80, v3
	v_add_f32_e32 v74, 1.0, v74
	v_add_f32_e32 v75, 1.0, v75
	v_cvt_pk_fp8_f32 v80, v76, v77
	s_waitcnt lgkmcnt(0)
	v_add_f32_e32 v76, v82, v83
	v_rcp_f32_e32 v74, v74
	v_rcp_f32_e32 v75, v75
	v_mov_b32_e32 v81, v3
	ds_bpermute_b32 v77, v171, v76
	v_cvt_pk_fp8_f32 v81, v68, v69
	v_pk_mul_f32 v[70:71], v[70:71], v[86:87] op_sel_hi:[1,0]
	v_cvt_pk_fp8_f32 v80, v78, v79 op_sel:[0,0,1]
	v_pk_mul_f32 v[68:69], v[72:73], v[70:71]
	s_nop 0
	v_pk_mul_f32 v[68:69], v[68:69], v[74:75]
	s_nop 0
	v_cvt_pk_fp8_f32 v81, v68, v69 op_sel:[0,0,1]
	s_waitcnt lgkmcnt(0)
; __device__ __forceinline__ float rstd_fin4(const f32x4 a) { float s = (a[0] + a[1]) + (a[2] + a[3]); s += __shfl_xor(s, 16); s += __shfl_xor(s, 32); return __builtin_amdgcn_rsqf(s * (1.f / 1024.f) + 1e-6f); }
;     __device__ __forceinline__ void operator()(const f32x4 (&acc)[2][2][4][2], const Unit& u, int wr, int wc, int fr, int fq) const {
;     ...
;             for (int m = 0; m < 4; ++m) { const float rs = rstd_fin4(pa[ai][m]) * sc;
;                 const float rsl = rs * 1.4426950408889634f, rsu = rs * 0.6931471805599453f;
;                 f32x4 h0, h1;
; #pragma unroll
;                 for (int n = 0; n < 2; ++n) { const f32x4 G = acc[ai][0][m][n], U = acc[ai][1][m][n]; f32x4 hv;
; #pragma unroll
;                     for (int q = 0; q < 2; ++q) { const f32x2 g2 = (f32x2){G[2 * q], G[2 * q + 1]} * rsl, u2 = (f32x2){U[2 * q], U[2 * q + 1]} * rsu;
;                         f32x2 r2; r2.x = __builtin_amdgcn_rcpf(1.f + __builtin_amdgcn_exp2f(-g2.x)); r2.y = __builtin_amdgcn_rcpf(1.f + __builtin_amdgcn_exp2f(-g2.y));
;                         const f32x2 o2 = g2 * u2 * r2; hv[2 * q] = o2.x; hv[2 * q + 1] = o2.y; }
;                     if (n == 0) h0 = hv; else h1 = hv; }
;                 unsigned w0 = 0u, w1 = 0u;
;                 w0 = __builtin_amdgcn_cvt_pk_fp8_f32(h0[0], h0[1], w0, false); w0 = __builtin_amdgcn_cvt_pk_fp8_f32(h0[2], h0[3], w0, true); w1 = __builtin_amdgcn_cvt_pk_fp8_f32(h1[0], h1[1], w1, false); w1 = __builtin_amdgcn_cvt_pk_fp8_f32(h1[2], h1[3], w1, true);
;                 *(u32x2*)(hb + (ai * 4 + m) * 512) = (u32x2){w0, w1}; asm volatile("" ::: "memory"); }
	v_add_f32_e32 v68, v76, v77
	v_fmamk_f32 v68, v68, 0x3a800000, v227
	v_rsq_f32_e32 v69, v68
	v_mov_b32_e32 v212, v80
	v_mov_b32_e32 v213, v81
	s_nop 1
	v_permlane16_swap_b32_e32 v212, v214
	v_permlane16_swap_b32_e32 v213, v215
	global_store_dwordx4 v[216:217], v[212:215], off offset:1024
	v_mul_f32_e32 v68, 0x3fb8aa3b, v69
	v_pk_mul_f32 v[64:65], v[64:65], v[68:69] op_sel_hi:[1,0]
	v_mul_f32_e32 v70, 0x3f317218, v69
	v_exp_f32_e64 v71, -v64
	v_exp_f32_e64 v69, -v65
	v_pk_mul_f32 v[60:61], v[60:61], v[70:71] op_sel_hi:[1,0]
	v_add_f32_e32 v69, 1.0, v69
	v_pk_mul_f32 v[60:61], v[64:65], v[60:61]
	v_pk_mul_f32 v[64:65], v[66:67], v[68:69] op_sel_hi:[1,0]
	v_add_f32_e32 v71, 1.0, v71
	v_exp_f32_e64 v66, -v64
	v_exp_f32_e64 v67, -v65
	v_pk_mul_f32 v[62:63], v[62:63], v[70:71] op_sel_hi:[1,0]
	v_pk_mul_f32 v[56:57], v[56:57], v[68:69] op_sel_hi:[1,0]
	v_add_f32_e32 v66, 1.0, v66
	v_add_f32_e32 v67, 1.0, v67
	v_pk_mul_f32 v[62:63], v[64:65], v[62:63]
	v_exp_f32_e64 v64, -v56
	v_exp_f32_e64 v65, -v57
	v_rcp_f32_e32 v66, v66
	v_rcp_f32_e32 v67, v67
	v_add_f32_e32 v64, 1.0, v64
	v_add_f32_e32 v65, 1.0, v65
	v_pk_mul_f32 v[58:59], v[58:59], v[68:69] op_sel_hi:[1,0]
	v_pk_mul_f32 v[62:63], v[62:63], v[66:67]
	v_rcp_f32_e32 v64, v64
	v_rcp_f32_e32 v65, v65
	v_exp_f32_e64 v66, -v58
	v_pk_mul_f32 v[52:53], v[52:53], v[70:71] op_sel_hi:[1,0]
	v_rcp_f32_e32 v72, v71
	v_pk_mul_f32 v[52:53], v[56:57], v[52:53]
	s_waitcnt vmcnt(4)
	v_mov_b32_e32 v56, v141
	v_mov_b32_e32 v57, v142
	v_mov_b32_e32 v141, v143
	v_pk_add_f32 v[56:57], v[56:57], v[140:141]
	v_pk_mul_f32 v[52:53], v[52:53], v[64:65]
	v_add_f32_e32 v64, 1.0, v66
	v_add_f32_e32 v66, v56, v57
	ds_bpermute_b32 v67, v172, v66
	v_exp_f32_e64 v65, -v59
	v_rcp_f32_e32 v56, v64
	v_rcp_f32_e32 v73, v69
	v_pk_mul_f32 v[54:55], v[54:55], v[70:71] op_sel_hi:[1,0]
	s_waitcnt lgkmcnt(0)
	v_add_f32_e32 v64, v66, v67
	v_add_f32_e32 v57, 1.0, v65
	ds_bpermute_b32 v65, v171, v64
	v_pk_mul_f32 v[54:55], v[58:59], v[54:55]
	v_mov_b32_e32 v59, v3
	v_cvt_pk_fp8_f32 v59, v52, v53
	v_pk_mul_f32 v[60:61], v[60:61], v[72:73]
	s_waitcnt lgkmcnt(0)
	v_add_f32_e32 v52, v64, v65
	v_rcp_f32_e32 v57, v57
	v_mov_b32_e32 v58, v3
	v_fmamk_f32 v52, v52, 0x3a800000, v227
	v_cvt_pk_fp8_f32 v58, v60, v61
	v_rsq_f32_e32 v60, v52
	v_pk_mul_f32 v[52:53], v[54:55], v[56:57]
	v_cvt_pk_fp8_f32 v58, v62, v63 op_sel:[0,0,1]
	v_cvt_pk_fp8_f32 v59, v52, v53 op_sel:[0,0,1]
	v_mul_f32_e32 v52, 0x3fb8aa3b, v60
	v_pk_mul_f32 v[48:49], v[48:49], v[52:53] op_sel_hi:[1,0]
	v_mul_f32_e32 v54, 0x3f317218, v60
	v_exp_f32_e64 v53, -v48
	v_exp_f32_e64 v55, -v49
	v_mov_b32_e32 v210, v58
	v_mov_b32_e32 v211, v59
	v_add_f32_e32 v53, 1.0, v53
	v_pk_mul_f32 v[44:45], v[44:45], v[54:55] op_sel_hi:[1,0]
	v_rcp_f32_e32 v56, v53
	v_add_f32_e32 v53, 1.0, v55
	v_pk_mul_f32 v[44:45], v[48:49], v[44:45]
	v_pk_mul_f32 v[48:49], v[50:51], v[52:53] op_sel_hi:[1,0]
	v_pk_mul_f32 v[46:47], v[46:47], v[54:55] op_sel_hi:[1,0]
	v_pk_mul_f32 v[40:41], v[40:41], v[52:53] op_sel_hi:[1,0]
	v_exp_f32_e64 v50, -v48
	v_exp_f32_e64 v51, -v49
	v_pk_mul_f32 v[46:47], v[48:49], v[46:47]
	v_exp_f32_e64 v48, -v40
	v_exp_f32_e64 v49, -v41
	v_add_f32_e32 v50, 1.0, v50
	v_add_f32_e32 v51, 1.0, v51
	v_add_f32_e32 v48, 1.0, v48
	v_add_f32_e32 v49, 1.0, v49
	v_rcp_f32_e32 v48, v48
	v_rcp_f32_e32 v49, v49
	v_rcp_f32_e32 v50, v50
	v_rcp_f32_e32 v51, v51
	v_pk_mul_f32 v[36:37], v[36:37], v[54:55] op_sel_hi:[1,0]
	v_rcp_f32_e32 v57, v53
	v_pk_mul_f32 v[36:37], v[40:41], v[36:37]
	v_pk_mul_f32 v[46:47], v[46:47], v[50:51]
	v_pk_mul_f32 v[36:37], v[36:37], v[48:49]
	s_waitcnt vmcnt(3)
	v_mov_b32_e32 v48, v137
	v_mov_b32_e32 v49, v138
	v_mov_b32_e32 v137, v139
	v_pk_add_f32 v[48:49], v[48:49], v[136:137]
	v_pk_mul_f32 v[40:41], v[42:43], v[52:53] op_sel_hi:[1,0]
	v_add_f32_e32 v50, v48, v49
	ds_bpermute_b32 v51, v172, v50
	v_exp_f32_e64 v42, -v40
	v_exp_f32_e64 v43, -v41
	v_pk_mul_f32 v[44:45], v[44:45], v[56:57]
	v_mov_b32_e32 v48, v3
	v_add_f32_e32 v42, 1.0, v42
	v_add_f32_e32 v43, 1.0, v43
	v_cvt_pk_fp8_f32 v48, v44, v45
	s_waitcnt lgkmcnt(0)
	v_add_f32_e32 v44, v50, v51
	v_rcp_f32_e32 v42, v42
	v_rcp_f32_e32 v43, v43
	v_mov_b32_e32 v49, v3
	ds_bpermute_b32 v45, v171, v44
	v_cvt_pk_fp8_f32 v49, v36, v37
	v_pk_mul_f32 v[38:39], v[38:39], v[54:55] op_sel_hi:[1,0]
	v_cvt_pk_fp8_f32 v48, v46, v47 op_sel:[0,0,1]
	v_pk_mul_f32 v[36:37], v[40:41], v[38:39]
	s_nop 0
	v_pk_mul_f32 v[36:37], v[36:37], v[42:43]
	s_nop 0
	v_cvt_pk_fp8_f32 v49, v36, v37 op_sel:[0,0,1]
	s_waitcnt lgkmcnt(0)
; __device__ __forceinline__ float rstd_fin4(const f32x4 a) { float s = (a[0] + a[1]) + (a[2] + a[3]); s += __shfl_xor(s, 16); s += __shfl_xor(s, 32); return __builtin_amdgcn_rsqf(s * (1.f / 1024.f) + 1e-6f); }
;     __device__ __forceinline__ void operator()(const f32x4 (&acc)[2][2][4][2], const Unit& u, int wr, int wc, int fr, int fq) const {
;     ...
;             for (int m = 0; m < 4; ++m) { const float rs = rstd_fin4(pa[ai][m]) * sc;
;                 const float rsl = rs * 1.4426950408889634f, rsu = rs * 0.6931471805599453f;
;                 f32x4 h0, h1;
; #pragma unroll
;                 for (int n = 0; n < 2; ++n) { const f32x4 G = acc[ai][0][m][n], U = acc[ai][1][m][n]; f32x4 hv;
; #pragma unroll
;                     for (int q = 0; q < 2; ++q) { const f32x2 g2 = (f32x2){G[2 * q], G[2 * q + 1]} * rsl, u2 = (f32x2){U[2 * q], U[2 * q + 1]} * rsu;
;                         f32x2 r2; r2.x = __builtin_amdgcn_rcpf(1.f + __builtin_amdgcn_exp2f(-g2.x)); r2.y = __builtin_amdgcn_rcpf(1.f + __builtin_amdgcn_exp2f(-g2.y));
;                         const f32x2 o2 = g2 * u2 * r2; hv[2 * q] = o2.x; hv[2 * q + 1] = o2.y; }
;                     if (n == 0) h0 = hv; else h1 = hv; }
;                 unsigned w0 = 0u, w1 = 0u;
;                 w0 = __builtin_amdgcn_cvt_pk_fp8_f32(h0[0], h0[1], w0, false); w0 = __builtin_amdgcn_cvt_pk_fp8_f32(h0[2], h0[3], w0, true); w1 = __builtin_amdgcn_cvt_pk_fp8_f32(h1[0], h1[1], w1, false); w1 = __builtin_amdgcn_cvt_pk_fp8_f32(h1[2], h1[3], w1, true);
;                 *(u32x2*)(hb + (ai * 4 + m) * 512) = (u32x2){w0, w1}; asm volatile("" ::: "memory"); }
	v_add_f32_e32 v36, v44, v45
	v_fmamk_f32 v36, v36, 0x3a800000, v227
	v_rsq_f32_e32 v37, v36
	v_mov_b32_e32 v208, v48
	v_mov_b32_e32 v209, v49
	s_nop 1
	v_permlane16_swap_b32_e32 v208, v210
	v_permlane16_swap_b32_e32 v209, v211
	global_store_dwordx4 v[216:217], v[208:211], off offset:2048
	v_mul_f32_e32 v36, 0x3fb8aa3b, v37
	v_pk_mul_f32 v[32:33], v[32:33], v[36:37] op_sel_hi:[1,0]
	v_mul_f32_e32 v38, 0x3f317218, v37
	v_exp_f32_e64 v39, -v32
	v_exp_f32_e64 v37, -v33
	v_pk_mul_f32 v[28:29], v[28:29], v[38:39] op_sel_hi:[1,0]
	v_add_f32_e32 v37, 1.0, v37
	v_pk_mul_f32 v[28:29], v[32:33], v[28:29]
	v_pk_mul_f32 v[32:33], v[34:35], v[36:37] op_sel_hi:[1,0]
	v_add_f32_e32 v39, 1.0, v39
	v_exp_f32_e64 v34, -v32
	v_exp_f32_e64 v35, -v33
	v_pk_mul_f32 v[30:31], v[30:31], v[38:39] op_sel_hi:[1,0]
	v_pk_mul_f32 v[24:25], v[24:25], v[36:37] op_sel_hi:[1,0]
	v_add_f32_e32 v34, 1.0, v34
	v_add_f32_e32 v35, 1.0, v35
	v_pk_mul_f32 v[30:31], v[32:33], v[30:31]
	v_exp_f32_e64 v32, -v24
	v_exp_f32_e64 v33, -v25
	v_rcp_f32_e32 v34, v34
	v_rcp_f32_e32 v35, v35
	v_add_f32_e32 v32, 1.0, v32
	v_add_f32_e32 v33, 1.0, v33
	v_pk_mul_f32 v[26:27], v[26:27], v[36:37] op_sel_hi:[1,0]
	v_pk_mul_f32 v[30:31], v[30:31], v[34:35]
	v_rcp_f32_e32 v32, v32
	v_rcp_f32_e32 v33, v33
	v_exp_f32_e64 v34, -v26
	v_pk_mul_f32 v[20:21], v[20:21], v[38:39] op_sel_hi:[1,0]
	v_rcp_f32_e32 v40, v39
	v_pk_mul_f32 v[20:21], v[24:25], v[20:21]
	s_waitcnt vmcnt(3)
	v_mov_b32_e32 v24, v125
	v_mov_b32_e32 v25, v126
	v_mov_b32_e32 v125, v127
	v_pk_add_f32 v[24:25], v[24:25], v[124:125]
	v_pk_mul_f32 v[20:21], v[20:21], v[32:33]
	v_add_f32_e32 v32, 1.0, v34
	v_add_f32_e32 v34, v24, v25
	ds_bpermute_b32 v35, v172, v34
	v_exp_f32_e64 v33, -v27
	v_rcp_f32_e32 v24, v32
	v_rcp_f32_e32 v41, v37
	v_pk_mul_f32 v[22:23], v[22:23], v[38:39] op_sel_hi:[1,0]
	s_waitcnt lgkmcnt(0)
	v_add_f32_e32 v32, v34, v35
	v_add_f32_e32 v25, 1.0, v33
	ds_bpermute_b32 v33, v171, v32
	v_pk_mul_f32 v[22:23], v[26:27], v[22:23]
	v_mov_b32_e32 v27, v3
	v_cvt_pk_fp8_f32 v27, v20, v21
	v_pk_mul_f32 v[28:29], v[28:29], v[40:41]
	s_waitcnt lgkmcnt(0)
	v_add_f32_e32 v20, v32, v33
	v_rcp_f32_e32 v25, v25
	v_mov_b32_e32 v26, v3
	v_fmamk_f32 v20, v20, 0x3a800000, v227
	v_cvt_pk_fp8_f32 v26, v28, v29
	v_rsq_f32_e32 v28, v20
	v_pk_mul_f32 v[20:21], v[22:23], v[24:25]
	v_cvt_pk_fp8_f32 v26, v30, v31 op_sel:[0,0,1]
	v_cvt_pk_fp8_f32 v27, v20, v21 op_sel:[0,0,1]
	v_mul_f32_e32 v20, 0x3fb8aa3b, v28
	v_pk_mul_f32 v[16:17], v[16:17], v[20:21] op_sel_hi:[1,0]
	v_mul_f32_e32 v22, 0x3f317218, v28
	v_exp_f32_e64 v21, -v16
	v_exp_f32_e64 v23, -v17
	v_mov_b32_e32 v214, v26
	v_mov_b32_e32 v215, v27
	v_add_f32_e32 v21, 1.0, v21
	v_pk_mul_f32 v[12:13], v[12:13], v[22:23] op_sel_hi:[1,0]
	v_rcp_f32_e32 v24, v21
	v_add_f32_e32 v21, 1.0, v23
	v_pk_mul_f32 v[12:13], v[16:17], v[12:13]
	v_pk_mul_f32 v[16:17], v[18:19], v[20:21] op_sel_hi:[1,0]
	v_pk_mul_f32 v[14:15], v[14:15], v[22:23] op_sel_hi:[1,0]
	v_pk_mul_f32 v[8:9], v[8:9], v[20:21] op_sel_hi:[1,0]
	v_exp_f32_e64 v18, -v16
	v_exp_f32_e64 v19, -v17
	v_pk_mul_f32 v[14:15], v[16:17], v[14:15]
	v_exp_f32_e64 v16, -v8
	v_exp_f32_e64 v17, -v9
	v_pk_mul_f32 v[4:5], v[4:5], v[22:23] op_sel_hi:[1,0]
	v_rcp_f32_e32 v25, v21
	v_pk_mul_f32 v[4:5], v[8:9], v[4:5]
	v_pk_mul_f32 v[8:9], v[10:11], v[20:21] op_sel_hi:[1,0]
	v_add_f32_e32 v16, 1.0, v16
	v_add_f32_e32 v17, 1.0, v17
	v_exp_f32_e64 v10, -v8
	v_exp_f32_e64 v11, -v9
	v_rcp_f32_e32 v16, v16
	v_rcp_f32_e32 v17, v17
	v_add_f32_e32 v18, 1.0, v18
	v_add_f32_e32 v19, 1.0, v19
	v_add_f32_e32 v10, 1.0, v10
	v_add_f32_e32 v11, 1.0, v11
	v_pk_mul_f32 v[12:13], v[12:13], v[24:25]
	v_rcp_f32_e32 v18, v18
	v_rcp_f32_e32 v19, v19
	v_pk_mul_f32 v[4:5], v[4:5], v[16:17]
	v_rcp_f32_e32 v10, v10
	v_rcp_f32_e32 v11, v11
	v_mov_b32_e32 v16, v3
	v_mov_b32_e32 v17, v3
	v_cvt_pk_fp8_f32 v16, v12, v13
	v_cvt_pk_fp8_f32 v17, v4, v5
	v_pk_mul_f32 v[6:7], v[6:7], v[22:23] op_sel_hi:[1,0]
	v_pk_mul_f32 v[14:15], v[14:15], v[18:19]
	v_pk_mul_f32 v[4:5], v[8:9], v[6:7]
	v_cvt_pk_fp8_f32 v16, v14, v15 op_sel:[0,0,1]
	v_pk_mul_f32 v[4:5], v[4:5], v[10:11]
	s_nop 0
	v_cvt_pk_fp8_f32 v17, v4, v5 op_sel:[0,0,1]
	v_mov_b32_e32 v212, v16
	v_mov_b32_e32 v213, v17
	s_nop 1
	v_permlane16_swap_b32_e32 v212, v214
	v_permlane16_swap_b32_e32 v213, v215
	global_store_dwordx4 v[216:217], v[212:215], off offset:3072
	s_cbranch_vccnz .LBB0_1701
	s_andn2_b64 vcc, exec, s[46:47]
	s_cbranch_vccnz .LBB0_1700
	s_barrier
	s_branch .LBB0_1700
